# full-row dwordx4 epilogue stores (LDS transpose) in all six GEMM kernels
# speedup vs baseline: 1.0513x; 1.0023x over previous
.LBB5_17:
	s_lshl_b64 s[10:11], s[10:11], 1
	s_add_u32 s10, s6, s10
	s_addc_u32 s11, s7, s11
	s_lshl_b32 s12, s23, 1
	s_add_u32 s10, s10, s12
	s_addc_u32 s11, s11, 0
	v_lshlrev_b32_e32 v76, 1, v75
	v_mov_b32_e32 v77, 0
	v_lshl_add_u64 v[76:77], s[10:11], 0, v[76:77]
	v_cmp_gt_u32_e32 vcc, s20, v68
	v_mbcnt_lo_u32_b32 v196, -1, 0
	v_mbcnt_hi_u32_b32 v196, -1, v196
	v_and_b32_e32 v197, 15, v196
	v_lshrrev_b32_e32 v198, 4, v196
	v_readfirstlane_b32 s36, v68
	s_nop 3
	s_cmp_ge_u32 s36, 48
	s_cselect_b32 s36, 2, 0
	s_lshr_b32 s37, s23, 6
	s_add_u32 s36, s36, s37
	s_mulk_i32 s36, 0x900
	s_add_u32 s36, s36, 0xa000
	v_mul_u32_u24_e32 v199, 0x90, v197
	v_lshl_add_u32 v199, v198, 3, v199
	v_add_u32_e32 v199, s36, v199
	v_lshrrev_b32_e32 v200, 3, v196
	v_and_b32_e32 v201, 7, v196
	v_mul_u32_u24_e32 v202, 0x90, v200
	v_lshl_add_u32 v202, v201, 4, v202
	v_add_u32_e32 v202, s36, v202
	v_lshlrev_b32_e32 v203, 2, v200
	v_add_u32_e32 v204, 32, v203
	v_lshlrev_b32_e32 v220, 4, v201
	v_mov_b32_e32 v221, 0
	v_sub_u32_e32 v205, v68, v197
	v_add_u32_e32 v205, v205, v200
	s_mov_b64 s[10:11], exec
	s_cbranch_execz .LBB5_19
	v_add_f32_e32 v63, v15, v63
	v_ashrrev_i32_e32 v75, 31, v74
	v_add_f32_e32 v62, v14, v62
	v_max_f32_e32 v69, 0, v63
	v_add_f32_e32 v63, v16, v64
	v_add_f32_e32 v64, v17, v65
	v_lshlrev_b64 v[74:75], 11, v[74:75]
	v_max_f32_e32 v62, 0, v62
	v_max_f32_e32 v63, 0, v63
	v_max_f32_e32 v64, 0, v64
	v_lshl_add_u64 v[74:75], v[76:77], 0, v[74:75]
	v_cvt_pk_f16_f32 v63, v63, v64
	v_cvt_pk_f16_f32 v62, v62, v69
	v_add_f32_e32 v59, v11, v59
	ds_write_b64 v199, v[62:63]
	v_add_f32_e32 v58, v10, v58
	v_max_f32_e32 v62, 0, v59
	v_add_f32_e32 v59, v12, v60
	v_add_f32_e32 v60, v13, v61
	v_max_f32_e32 v58, 0, v58
	v_max_f32_e32 v59, 0, v59
	v_max_f32_e32 v60, 0, v60
	v_cvt_pk_f16_f32 v59, v59, v60
	v_cvt_pk_f16_f32 v58, v58, v62
	v_add_f32_e32 v55, v7, v55
	ds_write_b64 v199, v[58:59] offset:32
	v_add_f32_e32 v54, v6, v54
	v_max_f32_e32 v58, 0, v55
	v_add_f32_e32 v55, v8, v56
	v_add_f32_e32 v56, v9, v57
	v_max_f32_e32 v54, 0, v54
	v_max_f32_e32 v55, 0, v55
	v_max_f32_e32 v56, 0, v56
	v_cvt_pk_f16_f32 v55, v55, v56
	v_cvt_pk_f16_f32 v54, v54, v58
	v_add_f32_e32 v47, v3, v47
	ds_write_b64 v199, v[54:55] offset:64
	v_add_f32_e32 v46, v2, v46
	v_max_f32_e32 v54, 0, v47
	v_add_f32_e32 v47, v4, v48
	v_add_f32_e32 v48, v5, v49
	v_max_f32_e32 v46, 0, v46
	v_max_f32_e32 v47, 0, v47
	v_max_f32_e32 v48, 0, v48
	v_cvt_pk_f16_f32 v47, v47, v48
	v_cvt_pk_f16_f32 v46, v46, v54
	ds_write_b64 v199, v[46:47] offset:96
	s_waitcnt lgkmcnt(0)
	ds_read_b128 v[208:211], v202
	ds_read_b128 v[212:215], v202 offset:1152
	ds_bpermute_b32 v216, v203, v74
	ds_bpermute_b32 v217, v203, v75
	ds_bpermute_b32 v218, v204, v74
	ds_bpermute_b32 v219, v204, v75
	v_add_u32_e32 v222, 0, v205
	v_cmp_gt_u32_e64 s[38:39], s20, v222
	v_add_u32_e32 v222, 8, v222
	v_cmp_gt_u32_e64 s[40:41], s20, v222
	s_waitcnt lgkmcnt(0)
	v_lshl_add_u64 v[216:217], v[216:217], 0, v[220:221]
	v_lshl_add_u64 v[218:219], v[218:219], 0, v[220:221]
	s_mov_b64 s[42:43], exec
	s_and_b64 exec, s[42:43], s[38:39]
	global_store_dwordx4 v[216:217], v[208:211], off
	s_and_b64 exec, s[42:43], s[40:41]
	global_store_dwordx4 v[218:219], v[212:215], off
	s_mov_b64 exec, s[42:43]
.LBB5_19:
	s_or_b64 exec, exec, s[10:11]
	v_add_u32_e32 v46, 16, v68
	v_cmp_gt_u32_e32 vcc, s20, v46
	s_mov_b64 s[10:11], exec
	s_cbranch_execz .LBB5_21
	v_add_f32_e32 v43, v15, v43
	v_ashrrev_i32_e32 v73, 31, v72
	v_add_f32_e32 v42, v14, v42
	v_max_f32_e32 v48, 0, v43
	v_add_f32_e32 v43, v16, v44
	v_add_f32_e32 v44, v17, v45
	v_lshlrev_b64 v[46:47], 11, v[72:73]
	v_max_f32_e32 v42, 0, v42
	v_max_f32_e32 v43, 0, v43
	v_max_f32_e32 v44, 0, v44
	v_lshl_add_u64 v[46:47], v[76:77], 0, v[46:47]
	v_cvt_pk_f16_f32 v43, v43, v44
	v_cvt_pk_f16_f32 v42, v42, v48
	v_add_f32_e32 v39, v11, v39
	ds_write_b64 v199, v[42:43]
	v_add_f32_e32 v38, v10, v38
	v_max_f32_e32 v42, 0, v39
	v_add_f32_e32 v39, v12, v40
	v_add_f32_e32 v40, v13, v41
	v_max_f32_e32 v38, 0, v38
	v_max_f32_e32 v39, 0, v39
	v_max_f32_e32 v40, 0, v40
	v_cvt_pk_f16_f32 v39, v39, v40
	v_cvt_pk_f16_f32 v38, v38, v42
	v_add_f32_e32 v35, v7, v35
	ds_write_b64 v199, v[38:39] offset:32
	v_add_f32_e32 v34, v6, v34
	v_max_f32_e32 v38, 0, v35
	v_add_f32_e32 v35, v8, v36
	v_add_f32_e32 v36, v9, v37
	v_max_f32_e32 v34, 0, v34
	v_max_f32_e32 v35, 0, v35
	v_max_f32_e32 v36, 0, v36
	v_cvt_pk_f16_f32 v35, v35, v36
	v_cvt_pk_f16_f32 v34, v34, v38
	v_add_f32_e32 v31, v3, v31
	ds_write_b64 v199, v[34:35] offset:64
	v_add_f32_e32 v30, v2, v30
	v_max_f32_e32 v34, 0, v31
	v_add_f32_e32 v31, v4, v32
	v_add_f32_e32 v32, v5, v33
	v_max_f32_e32 v30, 0, v30
	v_max_f32_e32 v31, 0, v31
	v_max_f32_e32 v32, 0, v32
	v_cvt_pk_f16_f32 v31, v31, v32
	v_cvt_pk_f16_f32 v30, v30, v34
	ds_write_b64 v199, v[30:31] offset:96
	s_waitcnt lgkmcnt(0)
	ds_read_b128 v[208:211], v202
	ds_read_b128 v[212:215], v202 offset:1152
	ds_bpermute_b32 v216, v203, v46
	ds_bpermute_b32 v217, v203, v47
	ds_bpermute_b32 v218, v204, v46
	ds_bpermute_b32 v219, v204, v47
	v_add_u32_e32 v222, 16, v205
	v_cmp_gt_u32_e64 s[38:39], s20, v222
	v_add_u32_e32 v222, 8, v222
	v_cmp_gt_u32_e64 s[40:41], s20, v222
	s_waitcnt lgkmcnt(0)
	v_lshl_add_u64 v[216:217], v[216:217], 0, v[220:221]
	v_lshl_add_u64 v[218:219], v[218:219], 0, v[220:221]
	s_mov_b64 s[42:43], exec
	s_and_b64 exec, s[42:43], s[38:39]
	global_store_dwordx4 v[216:217], v[208:211], off
	s_and_b64 exec, s[42:43], s[40:41]
	global_store_dwordx4 v[218:219], v[212:215], off
	s_mov_b64 exec, s[42:43]
.LBB5_21:
	s_or_b64 exec, exec, s[10:11]
	v_add_u32_e32 v30, 32, v68
	v_cmp_gt_u32_e32 vcc, s20, v30
	s_mov_b64 s[10:11], exec
	s_cbranch_execz .LBB5_23
	v_add_f32_e32 v15, v15, v27
	v_ashrrev_i32_e32 v71, 31, v70
	v_add_f32_e32 v14, v14, v26
	v_max_f32_e32 v26, 0, v15
	v_add_f32_e32 v15, v16, v28
	v_add_f32_e32 v16, v17, v29
	v_lshlrev_b64 v[30:31], 11, v[70:71]
	v_max_f32_e32 v14, 0, v14
	v_max_f32_e32 v15, 0, v15
	v_max_f32_e32 v16, 0, v16
	v_lshl_add_u64 v[30:31], v[76:77], 0, v[30:31]
	v_cvt_pk_f16_f32 v15, v15, v16
	v_cvt_pk_f16_f32 v14, v14, v26
	v_add_f32_e32 v11, v11, v23
	ds_write_b64 v199, v[14:15]
	v_add_f32_e32 v10, v10, v22
	v_max_f32_e32 v14, 0, v11
	v_add_f32_e32 v11, v12, v24
	v_add_f32_e32 v12, v13, v25
	v_max_f32_e32 v10, 0, v10
	v_max_f32_e32 v11, 0, v11
	v_max_f32_e32 v12, 0, v12
	v_cvt_pk_f16_f32 v11, v11, v12
	v_cvt_pk_f16_f32 v10, v10, v14
	v_add_f32_e32 v7, v7, v19
	ds_write_b64 v199, v[10:11] offset:32
	v_add_f32_e32 v6, v6, v18
	v_max_f32_e32 v10, 0, v7
	v_add_f32_e32 v7, v8, v20
	v_add_f32_e32 v8, v9, v21
	v_max_f32_e32 v6, 0, v6
	v_max_f32_e32 v7, 0, v7
	v_max_f32_e32 v8, 0, v8
	v_cvt_pk_f16_f32 v7, v7, v8
	v_cvt_pk_f16_f32 v6, v6, v10
	v_add_f32_e32 v3, v3, v51
	ds_write_b64 v199, v[6:7] offset:64
	v_add_f32_e32 v2, v2, v50
	v_max_f32_e32 v6, 0, v3
	v_add_f32_e32 v3, v4, v52
	v_add_f32_e32 v4, v5, v53
	v_max_f32_e32 v2, 0, v2
	v_max_f32_e32 v3, 0, v3
	v_max_f32_e32 v4, 0, v4
	v_cvt_pk_f16_f32 v3, v3, v4
	v_cvt_pk_f16_f32 v2, v2, v6
	ds_write_b64 v199, v[2:3] offset:96
	s_waitcnt lgkmcnt(0)
	ds_read_b128 v[208:211], v202
	ds_read_b128 v[212:215], v202 offset:1152
	ds_bpermute_b32 v216, v203, v30
	ds_bpermute_b32 v217, v203, v31
	ds_bpermute_b32 v218, v204, v30
	ds_bpermute_b32 v219, v204, v31
	v_add_u32_e32 v222, 32, v205
	v_cmp_gt_u32_e64 s[38:39], s20, v222
	v_add_u32_e32 v222, 8, v222
	v_cmp_gt_u32_e64 s[40:41], s20, v222
	s_waitcnt lgkmcnt(0)
	v_lshl_add_u64 v[216:217], v[216:217], 0, v[220:221]
	v_lshl_add_u64 v[218:219], v[218:219], 0, v[220:221]
	s_mov_b64 s[42:43], exec
	s_and_b64 exec, s[42:43], s[38:39]
	global_store_dwordx4 v[216:217], v[208:211], off
	s_and_b64 exec, s[42:43], s[40:41]
	global_store_dwordx4 v[218:219], v[212:215], off
	s_mov_b64 exec, s[42:43]

.LBB5_26:
	s_mul_i32 s4, s13, 0xa000
	s_add_i32 s4, s4, 0
	v_add_u32_e32 v35, s4, v43
	s_add_i32 s4, s4, s12
	v_add_u32_e32 v80, s4, v41
	s_waitcnt vmcnt(5)
	s_barrier
	v_add_u32_e32 v60, v80, v39
	ds_read_b128 v[56:59], v60 offset:24576
	ds_read_b128 v[60:63], v60 offset:26624
	v_add_u32_e32 v68, v35, v39
	ds_read_b128 v[52:55], v68
	v_add_u32_e32 v35, v35, v37
	s_waitcnt lgkmcnt(0)
	v_mfma_f32_16x16x32_f16 v[26:29], v[56:59], v[52:55], v[26:29]
	ds_read_b128 v[64:67], v68 offset:2048
	v_add_u32_e32 v82, v80, v37
	s_cmp_gt_i32 s13, 0
	v_mfma_f32_16x16x32_f16 v[30:33], v[60:63], v[52:55], v[30:33]
	ds_read_b128 v[52:55], v68 offset:4096
	s_cselect_b32 s4, -1, 2
	s_add_i32 s4, s4, s13
	s_waitcnt lgkmcnt(0)
	v_mfma_f32_16x16x32_f16 v[22:25], v[56:59], v[64:67], v[22:25]
	ds_read_b128 v[68:71], v35
	s_mul_i32 s4, s4, 0xa000
	s_add_i32 s4, s9, s4
	v_mfma_f32_16x16x32_f16 v[18:21], v[60:63], v[64:67], v[18:21]
	ds_read_b128 v[64:67], v82 offset:24576
	v_lshl_add_u64 v[72:73], v[44:45], 0, s[2:3]
	s_mov_b32 m0, s4
	v_mfma_f32_16x16x32_f16 v[14:17], v[56:59], v[52:55], v[14:17]
	ds_read_b128 v[56:59], v82 offset:26624
	v_lshl_add_u64 v[74:75], v[46:47], 0, s[2:3]
	v_lshl_add_u64 v[76:77], v[0:1], 0, s[2:3]
	v_mfma_f32_16x16x32_f16 v[10:13], v[60:63], v[52:55], v[10:13]
	ds_read_b128 v[52:55], v35 offset:2048
	v_lshl_add_u64 v[78:79], v[48:49], 0, s[2:3]
	v_lshl_add_u64 v[80:81], v[50:51], 0, s[2:3]
	s_waitcnt lgkmcnt(0)
	v_mfma_f32_16x16x32_f16 v[26:29], v[64:67], v[68:71], v[26:29]
	ds_read_b128 v[60:63], v35 offset:4096
	v_mfma_f32_16x16x32_f16 v[30:33], v[56:59], v[68:71], v[30:33]
	global_load_lds_dwordx4 v[72:73], off
	s_add_i32 m0, s4, 0x1000
	v_mfma_f32_16x16x32_f16 v[22:25], v[64:67], v[52:55], v[22:25]
	global_load_lds_dwordx4 v[74:75], off
	s_add_i32 m0, s4, 0x2000
	v_mfma_f32_16x16x32_f16 v[18:21], v[56:59], v[52:55], v[18:21]
	global_load_lds_dwordx4 v[76:77], off
	s_add_i32 m0, s4, 0x6000
	s_waitcnt lgkmcnt(0)
	v_mfma_f32_16x16x32_f16 v[14:17], v[64:67], v[60:63], v[14:17]
	global_load_lds_dwordx4 v[78:79], off
	s_add_i32 m0, s4, 0x7000
	v_mfma_f32_16x16x32_f16 v[10:13], v[56:59], v[60:63], v[10:13]
	global_load_lds_dwordx4 v[80:81], off
	s_add_i32 s4, s13, 1
	s_cmp_lg_u32 s13, 2
	s_cselect_b32 s13, s4, 0
	s_add_u32 s2, s2, 0x80
	s_addc_u32 s3, s3, 0
	s_cmpk_lg_i32 s2, 0xf00
	s_cbranch_scc1 .LBB5_26
	s_add_i32 s2, s12, 0
	v_add_u32_e32 v0, s2, v41
	s_waitcnt vmcnt(5)
	s_barrier
	v_add_u32_e32 v1, v0, v39
	ds_read_b128 v[44:47], v1 offset:24576
	v_add_u32_e32 v35, 0, v43
	v_add_u32_e32 v43, v35, v39
	ds_read_b128 v[48:51], v43
	ds_read_b128 v[52:55], v1 offset:26624
	v_add_u32_e32 v1, v35, v37
	s_waitcnt lgkmcnt(0)
	v_mfma_f32_16x16x32_f16 v[26:29], v[44:47], v[48:51], v[26:29]
	ds_read_b128 v[56:59], v43 offset:2048
	v_add_u32_e32 v0, v0, v37
	s_add_i32 s2, s2, 0x10000
	v_mfma_f32_16x16x32_f16 v[30:33], v[52:55], v[48:51], v[30:33]
	ds_read_b128 v[48:51], v43 offset:4096
	s_lshl_b64 s[0:1], s[0:1], 1
	s_add_u32 s0, s6, s0
	s_waitcnt lgkmcnt(0)
	v_mfma_f32_16x16x32_f16 v[22:25], v[44:47], v[56:59], v[22:25]
	ds_read_b128 v[60:63], v1
	s_addc_u32 s1, s7, s1
	v_cmp_gt_u32_e32 vcc, s20, v34
	v_mfma_f32_16x16x32_f16 v[18:21], v[52:55], v[56:59], v[18:21]
	ds_read_b128 v[56:59], v0 offset:24576
	v_mfma_f32_16x16x32_f16 v[14:17], v[44:47], v[48:51], v[14:17]
	ds_read_b128 v[44:47], v0 offset:26624
	v_add_u32_e32 v0, s2, v41
	v_add_u32_e32 v35, v0, v39
	v_mfma_f32_16x16x32_f16 v[10:13], v[52:55], v[48:51], v[10:13]
	ds_read_b128 v[48:51], v1 offset:2048
	v_add_u32_e32 v0, v0, v37
	s_lshl_b32 s2, s8, 1
	s_waitcnt lgkmcnt(0)
	v_mfma_f32_16x16x32_f16 v[26:29], v[56:59], v[60:63], v[26:29]
	ds_read_b128 v[52:55], v1 offset:4096
	s_waitcnt vmcnt(0)
	s_barrier
	v_mfma_f32_16x16x32_f16 v[30:33], v[44:47], v[60:63], v[30:33]
	s_add_u32 s0, s0, s2
	s_addc_u32 s1, s1, 0
	v_mfma_f32_16x16x32_f16 v[22:25], v[56:59], v[48:51], v[22:25]
	v_mfma_f32_16x16x32_f16 v[18:21], v[44:47], v[48:51], v[18:21]
	s_waitcnt lgkmcnt(0)
	v_mfma_f32_16x16x32_f16 v[14:17], v[56:59], v[52:55], v[14:17]
	v_mfma_f32_16x16x32_f16 v[10:13], v[44:47], v[52:55], v[10:13]
	ds_read_b128 v[44:47], v35
	ds_read_b128 v[48:51], v43 offset:40960
	ds_read_b128 v[52:55], v35 offset:2048
	s_waitcnt lgkmcnt(0)
	v_mfma_f32_16x16x32_f16 v[26:29], v[44:47], v[48:51], v[26:29]
	ds_read_b128 v[56:59], v43 offset:43008
	v_mfma_f32_16x16x32_f16 v[48:51], v[52:55], v[48:51], v[30:33]
	s_nop 2
	ds_read_b128 v[30:33], v43 offset:45056
	s_waitcnt lgkmcnt(0)
	v_mfma_f32_16x16x32_f16 v[22:25], v[44:47], v[56:59], v[22:25]
	ds_read_b128 v[60:63], v1 offset:40960
	v_mfma_f32_16x16x32_f16 v[18:21], v[52:55], v[56:59], v[18:21]
	ds_read_b128 v[56:59], v0
	v_mfma_f32_16x16x32_f16 v[14:17], v[44:47], v[30:33], v[14:17]
	ds_read_b128 v[44:47], v0 offset:2048
	v_lshlrev_b32_e32 v0, 1, v42
	v_mfma_f32_16x16x32_f16 v[52:55], v[52:55], v[30:33], v[10:13]
	s_nop 2
	ds_read_b128 v[10:13], v1 offset:43008
	s_waitcnt lgkmcnt(0)
	v_mfma_f32_16x16x32_f16 v[30:33], v[56:59], v[60:63], v[26:29]
	ds_read_b128 v[64:67], v1 offset:45056
	v_mov_b32_e32 v1, 0
	v_lshl_add_u64 v[0:1], s[0:1], 0, v[0:1]
	v_mfma_f32_16x16x32_f16 v[26:29], v[44:47], v[60:63], v[48:51]
	v_mfma_f32_16x16x32_f16 v[22:25], v[56:59], v[10:13], v[22:25]
	v_mfma_f32_16x16x32_f16 v[18:21], v[44:47], v[10:13], v[18:21]
	s_waitcnt lgkmcnt(0)
	v_mfma_f32_16x16x32_f16 v[10:13], v[56:59], v[64:67], v[14:17]
	v_mfma_f32_16x16x32_f16 v[14:17], v[44:47], v[64:67], v[52:55]
	v_mbcnt_lo_u32_b32 v196, -1, 0
	v_mbcnt_hi_u32_b32 v196, -1, v196
	v_and_b32_e32 v197, 15, v196
	v_lshrrev_b32_e32 v198, 4, v196
	v_readfirstlane_b32 s36, v34
	s_nop 3
	s_cmp_ge_u32 s36, 48
	s_cselect_b32 s36, 2, 0
	s_add_u32 s36, s36, s18
	s_mulk_i32 s36, 0x500
	s_add_u32 s36, s36, 0x14000
	v_mul_u32_u24_e32 v199, 0x50, v197
	v_lshl_add_u32 v199, v198, 3, v199
	v_add_u32_e32 v199, s36, v199
	v_lshrrev_b32_e32 v200, 2, v196
	v_and_b32_e32 v201, 3, v196
	v_mul_u32_u24_e32 v202, 0x50, v200
	v_lshl_add_u32 v202, v201, 4, v202
	v_add_u32_e32 v202, s36, v202
	v_lshlrev_b32_e32 v203, 2, v200
	v_add_u32_e32 v204, 32, v203
	v_lshlrev_b32_e32 v220, 4, v201
	v_mov_b32_e32 v221, 0
	v_sub_u32_e32 v205, v34, v197
	v_add_u32_e32 v205, v205, v200
	s_mov_b64 s[0:1], exec
	s_cbranch_execz .LBB5_29
	v_add_f32_e32 v31, v7, v31
	s_waitcnt vmcnt(0)
	v_ashrrev_i32_e32 v41, 31, v40
	v_add_f32_e32 v30, v6, v30
	v_max_f32_e32 v35, 0, v31
	v_add_f32_e32 v31, v8, v32
	v_add_f32_e32 v32, v9, v33
	v_lshlrev_b64 v[40:41], 11, v[40:41]
	v_max_f32_e32 v30, 0, v30
	v_max_f32_e32 v31, 0, v31
	v_max_f32_e32 v32, 0, v32
	v_lshl_add_u64 v[40:41], v[0:1], 0, v[40:41]
	v_cvt_pk_f16_f32 v31, v31, v32
	v_cvt_pk_f16_f32 v30, v30, v35
	v_add_f32_e32 v27, v3, v27
	ds_write_b64 v199, v[30:31]
	v_add_f32_e32 v26, v2, v26
	v_max_f32_e32 v30, 0, v27
	v_add_f32_e32 v27, v4, v28
	v_add_f32_e32 v28, v5, v29
	v_max_f32_e32 v26, 0, v26
	v_max_f32_e32 v27, 0, v27
	v_max_f32_e32 v28, 0, v28
	v_cvt_pk_f16_f32 v27, v27, v28
	v_cvt_pk_f16_f32 v26, v26, v30
	ds_write_b64 v199, v[26:27] offset:32
	s_waitcnt lgkmcnt(0)
	ds_read_b128 v[208:211], v202
	ds_bpermute_b32 v216, v203, v40
	ds_bpermute_b32 v217, v203, v41
	v_add_u32_e32 v222, 0, v205
	v_cmp_gt_u32_e64 s[38:39], s20, v222
	s_waitcnt lgkmcnt(0)
	v_lshl_add_u64 v[216:217], v[216:217], 0, v[220:221]
	s_mov_b64 s[42:43], exec
	s_and_b64 exec, s[42:43], s[38:39]
	global_store_dwordx4 v[216:217], v[208:211], off
	s_mov_b64 exec, s[42:43]
.LBB5_29:
	s_or_b64 exec, exec, s[0:1]
	v_add_u32_e32 v26, 16, v34
	v_cmp_gt_u32_e32 vcc, s20, v26
	s_mov_b64 s[0:1], exec
	s_cbranch_execz .LBB5_31
	v_add_f32_e32 v23, v7, v23
	s_waitcnt vmcnt(0)
	v_ashrrev_i32_e32 v39, 31, v38
	v_add_f32_e32 v22, v6, v22
	v_max_f32_e32 v28, 0, v23
	v_add_f32_e32 v23, v8, v24
	v_add_f32_e32 v24, v9, v25
	v_lshlrev_b64 v[26:27], 11, v[38:39]
	v_max_f32_e32 v22, 0, v22
	v_max_f32_e32 v23, 0, v23
	v_max_f32_e32 v24, 0, v24
	v_lshl_add_u64 v[26:27], v[0:1], 0, v[26:27]
	v_cvt_pk_f16_f32 v23, v23, v24
	v_cvt_pk_f16_f32 v22, v22, v28
	v_add_f32_e32 v19, v3, v19
	ds_write_b64 v199, v[22:23]
	v_add_f32_e32 v18, v2, v18
	v_max_f32_e32 v22, 0, v19
	v_add_f32_e32 v19, v4, v20
	v_add_f32_e32 v20, v5, v21
	v_max_f32_e32 v18, 0, v18
	v_max_f32_e32 v19, 0, v19
	v_max_f32_e32 v20, 0, v20
	v_cvt_pk_f16_f32 v19, v19, v20
	v_cvt_pk_f16_f32 v18, v18, v22
	ds_write_b64 v199, v[18:19] offset:32
	s_waitcnt lgkmcnt(0)
	ds_read_b128 v[208:211], v202
	ds_bpermute_b32 v216, v203, v26
	ds_bpermute_b32 v217, v203, v27
	v_add_u32_e32 v222, 16, v205
	v_cmp_gt_u32_e64 s[38:39], s20, v222
	s_waitcnt lgkmcnt(0)
	v_lshl_add_u64 v[216:217], v[216:217], 0, v[220:221]
	s_mov_b64 s[42:43], exec
	s_and_b64 exec, s[42:43], s[38:39]
	global_store_dwordx4 v[216:217], v[208:211], off
	s_mov_b64 exec, s[42:43]
.LBB5_31:
	s_or_b64 exec, exec, s[0:1]
	v_add_u32_e32 v18, 32, v34
	v_cmp_gt_u32_e32 vcc, s20, v18
	s_mov_b64 s[0:1], exec
	s_cbranch_execz .LBB5_33
	v_add_f32_e32 v7, v7, v11
	s_waitcnt vmcnt(0)
	v_ashrrev_i32_e32 v37, 31, v36
	v_add_f32_e32 v6, v6, v10
	v_max_f32_e32 v10, 0, v7
	v_add_f32_e32 v7, v8, v12
	v_add_f32_e32 v8, v9, v13
	v_lshlrev_b64 v[18:19], 11, v[36:37]
	v_max_f32_e32 v6, 0, v6
	v_max_f32_e32 v7, 0, v7
	v_max_f32_e32 v8, 0, v8
	v_lshl_add_u64 v[0:1], v[0:1], 0, v[18:19]
	v_cvt_pk_f16_f32 v7, v7, v8
	v_cvt_pk_f16_f32 v6, v6, v10
	v_add_f32_e32 v3, v3, v15
	ds_write_b64 v199, v[6:7]
	v_add_f32_e32 v2, v2, v14
	v_max_f32_e32 v6, 0, v3
	v_add_f32_e32 v3, v4, v16
	v_add_f32_e32 v4, v5, v17
	v_max_f32_e32 v2, 0, v2
	v_max_f32_e32 v3, 0, v3
	v_max_f32_e32 v4, 0, v4
	v_cvt_pk_f16_f32 v3, v3, v4
	v_cvt_pk_f16_f32 v2, v2, v6
	ds_write_b64 v199, v[2:3] offset:32
	s_waitcnt lgkmcnt(0)
	ds_read_b128 v[208:211], v202
	ds_bpermute_b32 v216, v203, v0
	ds_bpermute_b32 v217, v203, v1
	v_add_u32_e32 v222, 32, v205
	v_cmp_gt_u32_e64 s[38:39], s20, v222
	s_waitcnt lgkmcnt(0)
	v_lshl_add_u64 v[216:217], v[216:217], 0, v[220:221]
	s_mov_b64 s[42:43], exec
	s_and_b64 exec, s[42:43], s[38:39]
	global_store_dwordx4 v[216:217], v[208:211], off
	s_mov_b64 exec, s[42:43]

	.amdhsa_kernel _Z15gemm_dma_kernelILi0ELi96ELi128ELi64ELi2ELi2ELi3EEvPKDF16_PDF16_PKiS4_S1_S1_PKf
		.amdhsa_group_segment_fixed_size 0
		.amdhsa_private_segment_fixed_size 0
		.amdhsa_kernarg_size 56
		.amdhsa_user_sgpr_count 2
		.amdhsa_user_sgpr_dispatch_ptr 0
		.amdhsa_user_sgpr_queue_ptr 0
		.amdhsa_user_sgpr_kernarg_segment_ptr 1
		.amdhsa_user_sgpr_dispatch_id 0
		.amdhsa_user_sgpr_kernarg_preload_length 0
		.amdhsa_user_sgpr_kernarg_preload_offset 0
		.amdhsa_user_sgpr_private_segment_size 0
		.amdhsa_uses_dynamic_stack 0
		.amdhsa_enable_private_segment 0
		.amdhsa_system_sgpr_workgroup_id_x 1
		.amdhsa_system_sgpr_workgroup_id_y 0
		.amdhsa_system_sgpr_workgroup_id_z 0
		.amdhsa_system_sgpr_workgroup_info 0
		.amdhsa_system_vgpr_workitem_id 0
		.amdhsa_next_free_vgpr 224
		.amdhsa_next_free_sgpr 44
		.amdhsa_accum_offset 224
		.amdhsa_reserve_vcc 1
		.amdhsa_float_round_mode_32 0
		.amdhsa_float_round_mode_16_64 0
		.amdhsa_float_denorm_mode_32 3
		.amdhsa_float_denorm_mode_16_64 3
		.amdhsa_dx10_clamp 1
		.amdhsa_ieee_mode 1
		.amdhsa_fp16_overflow 0
		.amdhsa_tg_split 0
		.amdhsa_exception_fp_ieee_invalid_op 0
		.amdhsa_exception_fp_denorm_src 0
		.amdhsa_exception_fp_ieee_div_zero 0
		.amdhsa_exception_fp_ieee_overflow 0
		.amdhsa_exception_fp_ieee_underflow 0
		.amdhsa_exception_fp_ieee_inexact 0
		.amdhsa_exception_int_div_zero 0
	.end_amdhsa_kernel

.LBB6_39:
	ds_read_b128 v[14:17], v180 offset:24576
	ds_read_b128 v[18:21], v179
	ds_read_b128 v[22:25], v179 offset:4096
	ds_read_b128 v[82:85], v180 offset:28672
	ds_read_b128 v[86:89], v181
	s_waitcnt vmcnt(10)
	v_pk_add_f16 v10, v34, v10
	v_pk_add_f16 v11, v35, v11
	s_waitcnt lgkmcnt(3)
	v_mfma_f32_16x16x32_f16 v[78:81], v[14:17], v[18:21], v[98:101]
	v_pk_add_f16 v12, v36, v12
	v_pk_add_f16 v13, v37, v13
	v_cndmask_b32_e64 v12, v36, v12, s[2:3]
	s_waitcnt lgkmcnt(1)
	v_mfma_f32_16x16x32_f16 v[18:21], v[82:85], v[18:21], v[90:93]
	ds_read_b128 v[98:101], v183 offset:24576
	v_cndmask_b32_e64 v13, v37, v13, s[2:3]
	v_cndmask_b32_e64 v11, v35, v11, s[2:3]
	v_mfma_f32_16x16x32_f16 v[90:93], v[14:17], v[22:25], v[94:97]
	v_cndmask_b32_e64 v10, v34, v10, s[2:3]
	v_cmp_gt_u32_e32 vcc, s18, v170
	s_nop 0
	ds_read_b128 v[94:97], v179 offset:8192
	v_mfma_f32_16x16x32_f16 v[22:25], v[82:85], v[22:25], v[110:113]
	s_waitcnt lgkmcnt(0)
	v_mfma_f32_16x16x32_f16 v[14:17], v[14:17], v[94:97], v[114:117]
	v_mfma_f32_16x16x32_f16 v[82:85], v[82:85], v[94:97], v[118:121]
	ds_read_b128 v[94:97], v183 offset:28672
	v_mfma_f32_16x16x32_f16 v[78:81], v[98:101], v[86:89], v[78:81]
	s_waitcnt lgkmcnt(0)
	v_mfma_f32_16x16x32_f16 v[18:21], v[94:97], v[86:89], v[18:21]
	ds_read_b128 v[86:89], v181 offset:4096
	ds_read_b128 v[102:105], v181 offset:8192
	s_waitcnt lgkmcnt(1)
	v_mfma_f32_16x16x32_f16 v[90:93], v[98:101], v[86:89], v[90:93]
	v_mfma_f32_16x16x32_f16 v[22:25], v[94:97], v[86:89], v[22:25]
	ds_read_b128 v[86:89], v184 offset:24576
	s_waitcnt lgkmcnt(1)
	v_mfma_f32_16x16x32_f16 v[14:17], v[98:101], v[102:105], v[14:17]
	v_mfma_f32_16x16x32_f16 v[82:85], v[94:97], v[102:105], v[82:85]
	ds_read_b128 v[94:97], v182
	ds_read_b128 v[98:101], v182 offset:4096
	ds_read_b128 v[102:105], v184 offset:28672
	ds_read_b128 v[106:109], v185
	s_waitcnt lgkmcnt(3)
	v_mfma_f32_16x16x32_f16 v[78:81], v[86:89], v[94:97], v[78:81]
	s_waitcnt lgkmcnt(1)
	v_mfma_f32_16x16x32_f16 v[18:21], v[102:105], v[94:97], v[18:21]
	ds_read_b128 v[94:97], v182 offset:8192
	v_mfma_f32_16x16x32_f16 v[90:93], v[86:89], v[98:101], v[90:93]
	s_waitcnt lgkmcnt(0)
	v_mfma_f32_16x16x32_f16 v[14:17], v[86:89], v[94:97], v[14:17]
	ds_read_b128 v[86:89], v186 offset:24576
	v_mfma_f32_16x16x32_f16 v[82:85], v[102:105], v[94:97], v[82:85]
	ds_read_b128 v[94:97], v186 offset:28672
	v_mfma_f32_16x16x32_f16 v[22:25], v[102:105], v[98:101], v[22:25]
	ds_read_b128 v[98:101], v185 offset:4096
	ds_read_b128 v[102:105], v185 offset:8192
	ds_write_b128 v151, v[10:13] offset:12288
	s_waitcnt vmcnt(9)
	v_pk_add_f16 v10, v38, v26
	v_pk_add_f16 v11, v39, v27
	v_pk_add_f16 v12, v40, v28
	v_pk_add_f16 v13, v41, v29
	v_cndmask_b32_e64 v12, v40, v12, s[2:3]
	v_cndmask_b32_e64 v13, v41, v13, s[2:3]
	v_cndmask_b32_e64 v11, v39, v11, s[2:3]
	v_cndmask_b32_e64 v10, v38, v10, s[2:3]
	ds_write_b128 v151, v[10:13] offset:16384
	s_waitcnt vmcnt(8)
	v_pk_add_f16 v10, v42, v30
	v_pk_add_f16 v11, v43, v31
	v_pk_add_f16 v12, v44, v32
	v_pk_add_f16 v13, v45, v33
	v_cndmask_b32_e64 v12, v44, v12, s[2:3]
	v_cndmask_b32_e64 v13, v45, v13, s[2:3]
	v_cndmask_b32_e64 v11, v43, v11, s[2:3]
	v_cndmask_b32_e64 v10, v42, v10, s[2:3]
	s_waitcnt lgkmcnt(3)
	v_mfma_f32_16x16x32_f16 v[90:93], v[86:89], v[98:101], v[90:93]
	s_lshl_b64 s[2:3], s[14:15], 1
	s_add_u32 s2, s10, s2
	s_addc_u32 s3, s11, s3
	v_mfma_f32_16x16x32_f16 v[22:25], v[94:97], v[98:101], v[22:25]
	v_add_u32_e32 v98, 0xe000, v151
	ds_write_b128 v151, v[10:13] offset:20480
	s_waitcnt vmcnt(7)
	ds_write_b128 v151, v[46:49] offset:57344
	s_waitcnt vmcnt(6)
	ds_write_b128 v151, v[50:53] offset:61440
	s_waitcnt vmcnt(5)
	ds_write_b128 v98, v[54:57] offset:8192
	s_waitcnt vmcnt(4)
	ds_write_b128 v98, v[58:61] offset:12288
	s_waitcnt vmcnt(3)
	ds_write_b128 v98, v[62:65] offset:16384
	s_waitcnt vmcnt(2)
	ds_write_b128 v98, v[66:69] offset:20480
	s_waitcnt vmcnt(1)
	ds_write_b128 v98, v[70:73] offset:24576
	s_waitcnt vmcnt(0)
	ds_write_b128 v98, v[74:77] offset:28672
	s_waitcnt lgkmcnt(0)
	s_barrier
	ds_read_b128 v[10:13], v180 offset:57344
	ds_read_b128 v[30:33], v179 offset:12288
	ds_read_b128 v[34:37], v179 offset:16384
	v_mfma_f32_16x16x32_f16 v[78:81], v[86:89], v[106:109], v[78:81]
	ds_read_b128 v[42:45], v180 offset:61440
	ds_read_b128 v[46:49], v181 offset:12288
	v_mfma_f32_16x16x32_f16 v[18:21], v[94:97], v[106:109], v[18:21]
	s_waitcnt lgkmcnt(3)
	v_mfma_f32_16x16x32_f16 v[38:41], v[10:13], v[30:33], v[78:81]
	s_waitcnt lgkmcnt(1)
	v_mfma_f32_16x16x32_f16 v[18:21], v[42:45], v[30:33], v[18:21]
	v_mfma_f32_16x16x32_f16 v[30:33], v[10:13], v[34:37], v[90:93]
	v_mfma_f32_16x16x32_f16 v[22:25], v[42:45], v[34:37], v[22:25]
	ds_read_b128 v[34:37], v179 offset:20480
	v_mfma_f32_16x16x32_f16 v[14:17], v[86:89], v[102:105], v[14:17]
	v_mfma_f32_16x16x32_f16 v[26:29], v[94:97], v[102:105], v[82:85]
	s_waitcnt lgkmcnt(0)
	v_mfma_f32_16x16x32_f16 v[10:13], v[10:13], v[34:37], v[14:17]
	s_nop 4
	ds_read_b128 v[14:17], v183 offset:57344
	v_mfma_f32_16x16x32_f16 v[26:29], v[42:45], v[34:37], v[26:29]
	ds_read_b128 v[34:37], v183 offset:61440
	s_waitcnt lgkmcnt(1)
	v_mfma_f32_16x16x32_f16 v[38:41], v[14:17], v[46:49], v[38:41]
	s_waitcnt lgkmcnt(0)
	v_mfma_f32_16x16x32_f16 v[18:21], v[34:37], v[46:49], v[18:21]
	ds_read_b128 v[42:45], v181 offset:16384
	ds_read_b128 v[46:49], v181 offset:20480
	s_waitcnt lgkmcnt(1)
	v_mfma_f32_16x16x32_f16 v[30:33], v[14:17], v[42:45], v[30:33]
	s_waitcnt lgkmcnt(0)
	v_mfma_f32_16x16x32_f16 v[10:13], v[14:17], v[46:49], v[10:13]
	ds_read_b128 v[14:17], v184 offset:57344
	v_mfma_f32_16x16x32_f16 v[22:25], v[34:37], v[42:45], v[22:25]
	v_mfma_f32_16x16x32_f16 v[26:29], v[34:37], v[46:49], v[26:29]
	ds_read_b128 v[34:37], v182 offset:12288
	ds_read_b128 v[42:45], v182 offset:16384
	ds_read_b128 v[46:49], v184 offset:61440
	ds_read_b128 v[50:53], v185 offset:12288
	ds_read_b128 v[54:57], v186 offset:61440
	s_waitcnt lgkmcnt(4)
	v_mfma_f32_16x16x32_f16 v[38:41], v[14:17], v[34:37], v[38:41]
	s_waitcnt lgkmcnt(2)
	v_mfma_f32_16x16x32_f16 v[18:21], v[46:49], v[34:37], v[18:21]
	v_mfma_f32_16x16x32_f16 v[34:37], v[14:17], v[42:45], v[30:33]
	v_mfma_f32_16x16x32_f16 v[42:45], v[46:49], v[42:45], v[22:25]
	s_nop 2
	ds_read_b128 v[22:25], v182 offset:20480
	s_waitcnt lgkmcnt(0)
	v_mfma_f32_16x16x32_f16 v[10:13], v[14:17], v[22:25], v[10:13]
	ds_read_b128 v[14:17], v186 offset:57344
	v_mfma_f32_16x16x32_f16 v[46:49], v[46:49], v[22:25], v[26:29]
	s_waitcnt lgkmcnt(0)
	v_mfma_f32_16x16x32_f16 v[30:33], v[14:17], v[50:53], v[38:41]
	v_mfma_f32_16x16x32_f16 v[26:29], v[54:57], v[50:53], v[18:21]
	s_nop 2
	ds_read_b128 v[18:21], v185 offset:16384
	ds_read_b128 v[38:41], v185 offset:20480
	s_waitcnt lgkmcnt(1)
	v_mfma_f32_16x16x32_f16 v[22:25], v[14:17], v[18:21], v[34:37]
	s_nop 2
	v_lshlrev_b32_e32 v34, 1, v149
	v_mov_b32_e32 v35, 0
	s_waitcnt lgkmcnt(0)
	v_mfma_f32_16x16x32_f16 v[14:17], v[14:17], v[38:41], v[10:13]
	s_nop 2
	v_lshl_add_u64 v[10:11], s[2:3], 0, v[34:35]
	v_lshlrev_b32_e32 v34, 1, v147
	v_mfma_f32_16x16x32_f16 v[18:21], v[54:57], v[18:21], v[42:45]
	v_lshl_add_u64 v[34:35], v[10:11], 0, v[34:35]
	v_mfma_f32_16x16x32_f16 v[10:13], v[54:57], v[38:41], v[46:49]
	v_mbcnt_lo_u32_b32 v196, -1, 0
	v_mbcnt_hi_u32_b32 v196, -1, v196
	v_and_b32_e32 v197, 15, v196
	v_lshrrev_b32_e32 v198, 4, v196
	v_lshrrev_b32_e32 v222, 10, v151
	s_nop 0
	v_readfirstlane_b32 s36, v222
	s_nop 3
	s_and_b32 s36, s36, 7
	s_mulk_i32 s36, 0x500
	s_add_u32 s36, s36, 0x6000
	v_mul_u32_u24_e32 v199, 0x50, v197
	v_lshl_add_u32 v199, v198, 3, v199
	v_add_u32_e32 v199, s36, v199
	v_lshrrev_b32_e32 v200, 2, v196
	v_and_b32_e32 v201, 3, v196
	v_mul_u32_u24_e32 v202, 0x50, v200
	v_lshl_add_u32 v202, v201, 4, v202
	v_add_u32_e32 v202, s36, v202
	v_lshlrev_b32_e32 v203, 2, v200
	v_add_u32_e32 v204, 32, v203
	v_lshlrev_b32_e32 v220, 4, v201
	v_mov_b32_e32 v221, 0
	v_sub_u32_e32 v205, v170, v197
	v_add_u32_e32 v205, v205, v200
	s_mov_b64 s[2:3], exec
	s_cbranch_execz .LBB6_41
	v_add_f32_e32 v31, v7, v31
	v_ashrrev_i32_e32 v153, 31, v152
	v_add_f32_e32 v30, v6, v30
	v_max_f32_e32 v38, 0, v31
	v_add_f32_e32 v31, v8, v32
	v_add_f32_e32 v32, v9, v33
	v_lshlrev_b64 v[36:37], 11, v[152:153]
	v_max_f32_e32 v30, 0, v30
	v_max_f32_e32 v31, 0, v31
	v_max_f32_e32 v32, 0, v32
	v_lshl_add_u64 v[36:37], v[34:35], 0, v[36:37]
	v_cvt_pk_f16_f32 v31, v31, v32
	v_cvt_pk_f16_f32 v30, v30, v38
	v_add_f32_e32 v27, v3, v27
	ds_write_b64 v199, v[30:31]
	v_add_f32_e32 v26, v2, v26
	v_max_f32_e32 v30, 0, v27
	v_add_f32_e32 v27, v4, v28
	v_add_f32_e32 v28, v5, v29
	v_max_f32_e32 v26, 0, v26
	v_max_f32_e32 v27, 0, v27
	v_max_f32_e32 v28, 0, v28
	v_cvt_pk_f16_f32 v27, v27, v28
	v_cvt_pk_f16_f32 v26, v26, v30
	ds_write_b64 v199, v[26:27] offset:32
	s_waitcnt lgkmcnt(0)
	ds_read_b128 v[208:211], v202
	ds_bpermute_b32 v216, v203, v36
	ds_bpermute_b32 v217, v203, v37
	v_add_u32_e32 v222, 0, v205
	v_cmp_gt_u32_e64 s[38:39], s18, v222
	s_waitcnt lgkmcnt(0)
	v_lshl_add_u64 v[216:217], v[216:217], 0, v[220:221]
	s_mov_b64 s[42:43], exec
	s_and_b64 exec, s[42:43], s[38:39]
	global_store_dwordx4 v[216:217], v[208:211], off
	s_mov_b64 exec, s[42:43]
.LBB6_41:
	s_or_b64 exec, exec, s[2:3]
	v_or_b32_e32 v26, 16, v170
	v_cmp_gt_u32_e32 vcc, s18, v26
	s_mov_b64 s[2:3], exec
	s_cbranch_execz .LBB6_43
	v_add_f32_e32 v23, v7, v23
	v_ashrrev_i32_e32 v151, 31, v150
	v_add_f32_e32 v22, v6, v22
	v_max_f32_e32 v28, 0, v23
	v_add_f32_e32 v23, v8, v24
	v_add_f32_e32 v24, v9, v25
	v_lshlrev_b64 v[26:27], 11, v[150:151]
	v_max_f32_e32 v22, 0, v22
	v_max_f32_e32 v23, 0, v23
	v_max_f32_e32 v24, 0, v24
	v_lshl_add_u64 v[26:27], v[34:35], 0, v[26:27]
	v_cvt_pk_f16_f32 v23, v23, v24
	v_cvt_pk_f16_f32 v22, v22, v28
	v_add_f32_e32 v19, v3, v19
	ds_write_b64 v199, v[22:23]
	v_add_f32_e32 v18, v2, v18
	v_max_f32_e32 v22, 0, v19
	v_add_f32_e32 v19, v4, v20
	v_add_f32_e32 v20, v5, v21
	v_max_f32_e32 v18, 0, v18
	v_max_f32_e32 v19, 0, v19
	v_max_f32_e32 v20, 0, v20
	v_cvt_pk_f16_f32 v19, v19, v20
	v_cvt_pk_f16_f32 v18, v18, v22
	ds_write_b64 v199, v[18:19] offset:32
	s_waitcnt lgkmcnt(0)
	ds_read_b128 v[208:211], v202
	ds_bpermute_b32 v216, v203, v26
	ds_bpermute_b32 v217, v203, v27
	v_add_u32_e32 v222, 16, v205
	v_cmp_gt_u32_e64 s[38:39], s18, v222
	s_waitcnt lgkmcnt(0)
	v_lshl_add_u64 v[216:217], v[216:217], 0, v[220:221]
	s_mov_b64 s[42:43], exec
	s_and_b64 exec, s[42:43], s[38:39]
	global_store_dwordx4 v[216:217], v[208:211], off
	s_mov_b64 exec, s[42:43]
.LBB6_43:
	s_or_b64 exec, exec, s[2:3]
	v_or_b32_e32 v18, 32, v170
	v_cmp_gt_u32_e32 vcc, s18, v18
	s_mov_b64 s[2:3], exec
	s_cbranch_execz .LBB6_45
	v_add_f32_e32 v7, v7, v15
	v_ashrrev_i32_e32 v149, 31, v148
	v_add_f32_e32 v6, v6, v14
	v_max_f32_e32 v14, 0, v7
	v_add_f32_e32 v7, v8, v16
	v_add_f32_e32 v8, v9, v17
	v_lshlrev_b64 v[18:19], 11, v[148:149]
	v_max_f32_e32 v6, 0, v6
	v_max_f32_e32 v7, 0, v7
	v_max_f32_e32 v8, 0, v8
	v_lshl_add_u64 v[18:19], v[34:35], 0, v[18:19]
	v_cvt_pk_f16_f32 v7, v7, v8
	v_cvt_pk_f16_f32 v6, v6, v14
	v_add_f32_e32 v3, v3, v11
	ds_write_b64 v199, v[6:7]
	v_add_f32_e32 v2, v2, v10
	v_max_f32_e32 v6, 0, v3
	v_add_f32_e32 v3, v4, v12
	v_add_f32_e32 v4, v5, v13
	v_max_f32_e32 v2, 0, v2
	v_max_f32_e32 v3, 0, v3
	v_max_f32_e32 v4, 0, v4
	v_cvt_pk_f16_f32 v3, v3, v4
	v_cvt_pk_f16_f32 v2, v2, v6
	ds_write_b64 v199, v[2:3] offset:32
	s_waitcnt lgkmcnt(0)
	ds_read_b128 v[208:211], v202
	ds_bpermute_b32 v216, v203, v18
	ds_bpermute_b32 v217, v203, v19
	v_add_u32_e32 v222, 32, v205
	v_cmp_gt_u32_e64 s[38:39], s18, v222
	s_waitcnt lgkmcnt(0)
	v_lshl_add_u64 v[216:217], v[216:217], 0, v[220:221]
	s_mov_b64 s[42:43], exec
	s_and_b64 exec, s[42:43], s[38:39]
	global_store_dwordx4 v[216:217], v[208:211], off
	s_mov_b64 exec, s[42:43]

	.amdhsa_kernel _Z11gemm_kernelILi0ELi48ELi128ELi64ELi1ELi4ELi2ELi2ELi128EEvPKDF16_PDF16_PKiS4_S1_S1_PKf
		.amdhsa_group_segment_fixed_size 0
		.amdhsa_private_segment_fixed_size 0
		.amdhsa_kernarg_size 56
		.amdhsa_user_sgpr_count 2
		.amdhsa_user_sgpr_dispatch_ptr 0
		.amdhsa_user_sgpr_queue_ptr 0
		.amdhsa_user_sgpr_kernarg_segment_ptr 1
		.amdhsa_user_sgpr_dispatch_id 0
		.amdhsa_user_sgpr_kernarg_preload_length 0
		.amdhsa_user_sgpr_kernarg_preload_offset 0
		.amdhsa_user_sgpr_private_segment_size 0
		.amdhsa_uses_dynamic_stack 0
		.amdhsa_enable_private_segment 0
		.amdhsa_system_sgpr_workgroup_id_x 1
		.amdhsa_system_sgpr_workgroup_id_y 0
		.amdhsa_system_sgpr_workgroup_id_z 0
		.amdhsa_system_sgpr_workgroup_info 0
		.amdhsa_system_vgpr_workitem_id 0
		.amdhsa_next_free_vgpr 224
		.amdhsa_next_free_sgpr 44
		.amdhsa_accum_offset 224
		.amdhsa_reserve_vcc 1
		.amdhsa_float_round_mode_32 0
		.amdhsa_float_round_mode_16_64 0
		.amdhsa_float_denorm_mode_32 3
		.amdhsa_float_denorm_mode_16_64 3
		.amdhsa_dx10_clamp 1
		.amdhsa_ieee_mode 1
		.amdhsa_fp16_overflow 0
		.amdhsa_tg_split 0
		.amdhsa_exception_fp_ieee_invalid_op 0
		.amdhsa_exception_fp_denorm_src 0
		.amdhsa_exception_fp_ieee_div_zero 0
		.amdhsa_exception_fp_ieee_overflow 0
		.amdhsa_exception_fp_ieee_underflow 0
		.amdhsa_exception_fp_ieee_inexact 0
		.amdhsa_exception_int_div_zero 0
	.end_amdhsa_kernel

.LBB7_4:
	s_andn2_b64 vcc, exec, s[6:7]
	s_cbranch_vccnz .LBB7_11
	s_cmpk_gt_i32 s4, 0x1fe
	s_cbranch_scc1 .LBB7_11
	s_load_dwordx2 s[2:3], s[0:1], 0x18
	s_ashr_i32 s5, s4, 31
	s_lshl_b64 s[6:7], s[4:5], 2
	s_waitcnt lgkmcnt(0)
	s_add_u32 s2, s2, s6
	s_addc_u32 s3, s3, s7
	s_load_dword s11, s[2:3], 0x0
	s_waitcnt lgkmcnt(0)
	s_cmp_lt_i32 s11, 0
	s_cbranch_scc1 .LBB7_11
	s_load_dwordx2 s[2:3], s[0:1], 0x10
	s_lshl_b32 s4, s4, 6
	s_ashr_i32 s5, s4, 31
	s_lshl_b64 s[8:9], s[4:5], 2
	v_lshrrev_b32_e32 v1, 4, v0
	s_load_dwordx4 s[4:7], s[0:1], 0x0
	s_waitcnt lgkmcnt(0)
	s_add_u32 s2, s2, s8
	s_addc_u32 s3, s3, s9
	v_lshlrev_b32_e32 v3, 2, v1
	global_load_dword v2, v3, s[2:3]
	global_load_dword v4, v3, s[2:3] offset:128
	s_load_dwordx2 s[12:13], s[0:1], 0x20
	s_load_dwordx2 s[8:9], s[0:1], 0x30
	v_and_b32_e32 v96, 15, v0
	v_mov_b32_e32 v25, 0
	v_lshlrev_b32_e32 v24, 4, v96
	s_and_b32 s1, s11, 0xff
	v_lshl_add_u64 v[6:7], s[4:5], 0, v[24:25]
	s_lshr_b32 s4, s11, 8
	s_lshl_b32 s0, s1, 21
	s_waitcnt lgkmcnt(0)
	s_add_u32 s12, s12, s0
	s_addc_u32 s13, s13, 0
	s_lshl_b32 s0, s10, 7
	v_or_b32_e32 v8, s0, v1
	v_ashrrev_i32_e32 v9, 31, v8
	v_lshlrev_b64 v[8:9], 11, v[8:9]
	v_lshl_add_u64 v[8:9], s[12:13], 0, v[8:9]
	s_mov_b32 s14, 0x10000
	v_lshl_add_u64 v[8:9], v[8:9], 0, v[24:25]
	v_add_co_u32_e32 v10, vcc, s14, v8
	s_mov_b32 s15, 0x20000
	s_nop 0
	v_addc_co_u32_e32 v11, vcc, 0, v9, vcc
	v_add_co_u32_e32 v12, vcc, s15, v8
	s_mov_b32 s16, 0x30000
	s_nop 0
	v_addc_co_u32_e32 v13, vcc, 0, v9, vcc
	v_add_co_u32_e32 v14, vcc, s16, v8
	global_load_dwordx4 v[32:35], v[8:9], off
	s_nop 0
	v_addc_co_u32_e32 v15, vcc, 0, v9, vcc
	global_load_dwordx4 v[36:39], v[10:11], off
	global_load_dwordx4 v[40:43], v[12:13], off
	global_load_dwordx4 v[44:47], v[14:15], off
	v_bfe_u32 v30, v0, 6, 2
	v_bfe_u32 v29, v0, 4, 2
	s_movk_i32 s5, 0xf0
	s_lshl_b32 s1, s1, 12
	v_lshlrev_b32_e32 v21, 8, v96
	v_lshlrev_b32_e32 v24, 7, v30
	s_waitcnt vmcnt(5)
	v_ashrrev_i32_e32 v3, 31, v2
	s_waitcnt vmcnt(4)
	v_ashrrev_i32_e32 v5, 31, v4
	v_lshlrev_b64 v[2:3], 11, v[2:3]
	v_lshlrev_b64 v[4:5], 11, v[4:5]
	v_lshl_add_u64 v[16:17], v[6:7], 0, v[2:3]
	v_lshl_add_u64 v[18:19], v[6:7], 0, v[4:5]
	global_load_dwordx4 v[48:51], v[16:17], off
	global_load_dwordx4 v[52:55], v[18:19], off
	global_load_dwordx4 v[56:59], v[16:17], off offset:256
	global_load_dwordx4 v[60:63], v[18:19], off offset:256
	global_load_dwordx4 v[64:67], v[8:9], off offset:256
	global_load_dwordx4 v[68:71], v[10:11], off offset:256
	global_load_dwordx4 v[72:75], v[12:13], off offset:256
	global_load_dwordx4 v[76:79], v[14:15], off offset:256
	v_lshrrev_b32_e32 v2, 8, v0
	v_xor_b32_e32 v0, v1, v0
	v_lshlrev_b32_e32 v3, 8, v1
	v_lshlrev_b32_e32 v0, 4, v0
	v_and_or_b32 v0, v0, s5, v3
	s_add_u32 s5, s8, s1
	s_addc_u32 s10, s9, 0
	s_ashr_i32 s1, s0, 31
	s_lshl_b64 s[8:9], s[0:1], 2
	s_add_u32 s8, s5, s8
	v_lshlrev_b32_e32 v4, 13, v30
	v_bitop3_b32 v1, v1, v96, 3 bitop3:0x6c
	s_addc_u32 s9, s10, s9
	v_lshl_or_b32 v27, v2, 5, v96
	v_add3_u32 v97, 0, v4, v21
	v_lshlrev_b32_e32 v100, 4, v1
	v_add_u32_e32 v20, 0, v0
	v_lshl_add_u64 v[0:1], s[8:9], 0, v[24:25]
	v_lshlrev_b32_e32 v24, 4, v29
	v_lshlrev_b32_e32 v28, 2, v27
	v_add_u32_e32 v31, v97, v100
	v_lshl_add_u64 v[22:23], v[0:1], 0, v[24:25]
	v_lshlrev_b32_e32 v80, 13, v2
	global_load_dword v26, v28, s[2:3] offset:64
	global_load_dwordx4 v[4:7], v[22:23], off
	global_load_dwordx4 v[0:3], v[22:23], off offset:64
	v_bitop3_b32 v23, v29, v96, 4 bitop3:0x36
	v_lshlrev_b32_e32 v101, 4, v23
	v_add3_u32 v22, 0, v80, v21
	v_add_u32_e32 v21, v22, v100
	v_add_u32_e32 v23, v22, v101
	v_bitop3_b32 v24, v29, v96, 8 bitop3:0x36
	v_lshlrev_b32_e32 v102, 4, v24
	v_add_u32_e32 v24, v22, v102
	v_add_u32_e32 v104, 0x8000, v97
	v_add_u32_e32 v116, 0x8000, v20
	s_lshl_b64 s[0:1], s[0:1], 1
	s_add_u32 s0, s6, s0
	s_addc_u32 s1, s7, s1
	v_cmp_gt_u32_e32 vcc, s4, v27
	s_waitcnt vmcnt(14)
	ds_write_b128 v20, v[32:35] offset:32768
	s_waitcnt vmcnt(13)
	ds_write_b128 v20, v[36:39] offset:40960
	s_waitcnt vmcnt(12)
	ds_write_b128 v20, v[40:43] offset:49152
	s_waitcnt vmcnt(11)
	ds_write_b128 v20, v[44:47] offset:57344
	s_waitcnt vmcnt(10)
	ds_write_b128 v20, v[48:51]
	s_waitcnt vmcnt(9)
	ds_write_b128 v20, v[52:55] offset:8192
	s_waitcnt lgkmcnt(0)
	s_barrier
	ds_read_b128 v[34:37], v31 offset:32768
	v_add_u32_e32 v32, v97, v101
	ds_read_b128 v[38:41], v31 offset:36864
	ds_read_b128 v[42:45], v21
	ds_read_b128 v[46:49], v21 offset:4096
	ds_read_b128 v[80:83], v32 offset:32768
	ds_read_b128 v[88:91], v23
	ds_read_b128 v[92:95], v32 offset:36864
	s_waitcnt lgkmcnt(4)
	v_mfma_f32_16x16x32_f16 v[50:53], v[34:37], v[42:45], 0
	v_bitop3_b32 v33, v29, v96, 12 bitop3:0x36
	v_lshlrev_b32_e32 v103, 4, v33
	v_add_u32_e32 v33, v97, v103
	v_mfma_f32_16x16x32_f16 v[42:45], v[38:41], v[42:45], 0
	v_add_u32_e32 v22, v22, v103
	s_waitcnt lgkmcnt(3)
	v_mfma_f32_16x16x32_f16 v[84:87], v[34:37], v[46:49], 0
	v_add_u32_e32 v35, v97, v102
	v_add_u32_e32 v34, v104, v100
	v_mfma_f32_16x16x32_f16 v[36:39], v[38:41], v[46:49], 0
	ds_read_b128 v[46:49], v23 offset:4096
	s_waitcnt lgkmcnt(2)
	v_mfma_f32_16x16x32_f16 v[50:53], v[80:83], v[88:91], v[50:53]
	s_waitcnt lgkmcnt(1)
	v_mfma_f32_16x16x32_f16 v[40:43], v[92:95], v[88:91], v[42:45]
	ds_read_b128 v[88:91], v35 offset:32768
	s_waitcnt lgkmcnt(1)
	v_mfma_f32_16x16x32_f16 v[80:83], v[80:83], v[46:49], v[84:87]
	s_nop 2
	ds_read_b128 v[84:87], v24
	ds_read_b128 v[96:99], v35 offset:36864
	v_mfma_f32_16x16x32_f16 v[36:39], v[92:95], v[46:49], v[36:39]
	ds_read_b128 v[44:47], v24 offset:4096
	s_waitcnt lgkmcnt(2)
	v_mfma_f32_16x16x32_f16 v[48:51], v[88:91], v[84:87], v[50:53]
	s_nop 2
	ds_read_b128 v[52:55], v22
	ds_read_b128 v[92:95], v22 offset:4096
	s_waitcnt vmcnt(8)
	ds_write_b128 v20, v[56:59] offset:16384
	s_waitcnt lgkmcnt(4)
	v_mfma_f32_16x16x32_f16 v[40:43], v[96:99], v[84:87], v[40:43]
	ds_read_b128 v[56:59], v33 offset:32768
	ds_read_b128 v[84:87], v33 offset:36864
	s_waitcnt vmcnt(7)
	ds_write_b128 v20, v[60:63] offset:24576
	s_waitcnt vmcnt(6)
	ds_write_b128 v116, v[64:67] offset:32768
	s_waitcnt vmcnt(5)
	ds_write_b128 v116, v[68:71] offset:40960
	s_waitcnt vmcnt(4)
	ds_write_b128 v116, v[72:75] offset:49152
	s_waitcnt lgkmcnt(9)
	v_mfma_f32_16x16x32_f16 v[60:63], v[88:91], v[44:47], v[80:83]
	s_waitcnt vmcnt(3)
	ds_write_b128 v116, v[76:79] offset:57344
	v_mfma_f32_16x16x32_f16 v[36:39], v[96:99], v[44:47], v[36:39]
	global_load_dwordx4 v[44:47], v[16:17], off offset:512
	global_load_dwordx4 v[64:67], v[18:19], off offset:512
	global_load_dwordx4 v[68:71], v[8:9], off offset:512
	global_load_dwordx4 v[72:75], v[10:11], off offset:512
	global_load_dwordx4 v[76:79], v[12:13], off offset:512
	global_load_dwordx4 v[80:83], v[14:15], off offset:512
	s_waitcnt lgkmcnt(0)
	v_mfma_f32_16x16x32_f16 v[48:51], v[56:59], v[52:55], v[48:51]
	s_barrier
	v_mfma_f32_16x16x32_f16 v[40:43], v[84:87], v[52:55], v[40:43]
	v_mfma_f32_16x16x32_f16 v[52:55], v[56:59], v[92:95], v[60:63]
	ds_read_b128 v[56:59], v34 offset:32768
	s_nop 1
	ds_read_b128 v[60:63], v34 offset:36864
	v_mfma_f32_16x16x32_f16 v[84:87], v[84:87], v[92:95], v[36:39]
	s_nop 2
	ds_read_b128 v[36:39], v21 offset:16384
	ds_read_b128 v[88:91], v21 offset:20480
	s_waitcnt lgkmcnt(1)
	v_mfma_f32_16x16x32_f16 v[48:51], v[56:59], v[36:39], v[48:51]
	v_mfma_f32_16x16x32_f16 v[38:41], v[60:63], v[36:39], v[40:43]
	v_add_u32_e32 v36, v104, v101
	v_add_u32_e32 v37, v104, v102
	s_waitcnt lgkmcnt(0)
	v_mfma_f32_16x16x32_f16 v[52:55], v[56:59], v[88:91], v[52:55]
	ds_read_b128 v[56:59], v36 offset:32768
	ds_read_b128 v[92:95], v36 offset:36864
	v_mfma_f32_16x16x32_f16 v[60:63], v[60:63], v[88:91], v[84:87]
	s_nop 2
	ds_read_b128 v[84:87], v23 offset:16384
	ds_read_b128 v[88:91], v23 offset:20480
	s_waitcnt lgkmcnt(1)
	v_mfma_f32_16x16x32_f16 v[48:51], v[56:59], v[84:87], v[48:51]
	v_mfma_f32_16x16x32_f16 v[38:41], v[92:95], v[84:87], v[38:41]
	s_waitcnt lgkmcnt(0)
	v_mfma_f32_16x16x32_f16 v[52:55], v[56:59], v[88:91], v[52:55]
	ds_read_b128 v[56:59], v37 offset:32768
	ds_read_b128 v[84:87], v37 offset:36864
	v_mfma_f32_16x16x32_f16 v[60:63], v[92:95], v[88:91], v[60:63]
	ds_read_b128 v[88:91], v24 offset:16384
	ds_read_b128 v[92:95], v24 offset:20480
	s_waitcnt lgkmcnt(1)
	v_mfma_f32_16x16x32_f16 v[40:43], v[84:87], v[88:91], v[38:41]
	s_nop 2
	v_add_u32_e32 v38, v104, v103
	v_mfma_f32_16x16x32_f16 v[48:51], v[56:59], v[88:91], v[48:51]
	s_waitcnt lgkmcnt(0)
	v_mfma_f32_16x16x32_f16 v[52:55], v[56:59], v[92:95], v[52:55]
	ds_read_b128 v[56:59], v38 offset:32768
	ds_read_b128 v[88:91], v38 offset:36864
	global_load_dwordx4 v[96:99], v[16:17], off offset:768
	v_mfma_f32_16x16x32_f16 v[60:63], v[84:87], v[92:95], v[60:63]
	ds_read_b128 v[84:87], v22 offset:16384
	ds_read_b128 v[92:95], v22 offset:20480
	global_load_dwordx4 v[100:103], v[18:19], off offset:768
	global_load_dwordx4 v[104:107], v[8:9], off offset:768
	global_load_dwordx4 v[108:111], v[10:11], off offset:768
	global_load_dwordx4 v[112:115], v[12:13], off offset:768
	s_waitcnt lgkmcnt(1)
	v_mfma_f32_16x16x32_f16 v[48:51], v[56:59], v[84:87], v[48:51]
	v_mfma_f32_16x16x32_f16 v[40:43], v[88:91], v[84:87], v[40:43]
	global_load_dwordx4 v[84:87], v[14:15], off offset:768
	s_waitcnt vmcnt(11)
	ds_write_b128 v20, v[44:47]
	s_waitcnt vmcnt(10)
	ds_write_b128 v20, v[64:67] offset:8192
	s_waitcnt vmcnt(9)
	ds_write_b128 v20, v[68:71] offset:32768
	s_waitcnt vmcnt(8)
	ds_write_b128 v20, v[72:75] offset:40960
	s_waitcnt vmcnt(7)
	ds_write_b128 v20, v[76:79] offset:49152
	s_waitcnt vmcnt(6)
	ds_write_b128 v20, v[80:83] offset:57344
	s_waitcnt lgkmcnt(0)
	s_barrier
	ds_read_b128 v[44:47], v31 offset:32768
	v_mfma_f32_16x16x32_f16 v[52:55], v[56:59], v[92:95], v[52:55]
	v_mfma_f32_16x16x32_f16 v[56:59], v[88:91], v[92:95], v[60:63]
	s_nop 2
	ds_read_b128 v[60:63], v31 offset:36864
	ds_read_b128 v[64:67], v21
	ds_read_b128 v[68:71], v21 offset:4096
	s_waitcnt lgkmcnt(1)
	v_mfma_f32_16x16x32_f16 v[48:51], v[44:47], v[64:67], v[48:51]
	v_mfma_f32_16x16x32_f16 v[40:43], v[60:63], v[64:67], v[40:43]
	s_waitcnt lgkmcnt(0)
	v_mfma_f32_16x16x32_f16 v[44:47], v[44:47], v[68:71], v[52:55]
	s_nop 2
	ds_read_b128 v[52:55], v32 offset:32768
	ds_read_b128 v[64:67], v32 offset:36864
	v_mfma_f32_16x16x32_f16 v[56:59], v[60:63], v[68:71], v[56:59]
	ds_read_b128 v[60:63], v23
	ds_read_b128 v[68:71], v23 offset:4096
	s_waitcnt lgkmcnt(1)
	v_mfma_f32_16x16x32_f16 v[48:51], v[52:55], v[60:63], v[48:51]
	v_mfma_f32_16x16x32_f16 v[40:43], v[64:67], v[60:63], v[40:43]
	s_waitcnt lgkmcnt(0)
	v_mfma_f32_16x16x32_f16 v[44:47], v[52:55], v[68:71], v[44:47]
	ds_read_b128 v[52:55], v35 offset:32768
	ds_read_b128 v[60:63], v35 offset:36864
	v_mfma_f32_16x16x32_f16 v[56:59], v[64:67], v[68:71], v[56:59]
	ds_read_b128 v[64:67], v24
	ds_read_b128 v[68:71], v24 offset:4096
	ds_read_b128 v[72:75], v22
	ds_read_b128 v[76:79], v22 offset:4096
	s_waitcnt vmcnt(5)
	ds_write_b128 v20, v[96:99] offset:16384
	s_waitcnt lgkmcnt(4)
	v_mfma_f32_16x16x32_f16 v[48:51], v[52:55], v[64:67], v[48:51]
	v_mfma_f32_16x16x32_f16 v[40:43], v[60:63], v[64:67], v[40:43]
	ds_read_b128 v[64:67], v33 offset:32768
	ds_read_b128 v[80:83], v33 offset:36864
	s_waitcnt vmcnt(4)
	ds_write_b128 v20, v[100:103] offset:24576
	s_waitcnt vmcnt(3)
	ds_write_b128 v116, v[104:107] offset:32768
	s_waitcnt vmcnt(2)
	ds_write_b128 v116, v[108:111] offset:40960
	s_waitcnt vmcnt(1)
	ds_write_b128 v116, v[112:115] offset:49152
	s_waitcnt lgkmcnt(9)
	v_mfma_f32_16x16x32_f16 v[44:47], v[52:55], v[68:71], v[44:47]
	s_waitcnt vmcnt(0)
	ds_write_b128 v116, v[84:87] offset:57344
	v_mfma_f32_16x16x32_f16 v[52:55], v[60:63], v[68:71], v[56:59]
	s_nop 2
	global_load_dwordx4 v[56:59], v[16:17], off offset:1024
	global_load_dwordx4 v[60:63], v[18:19], off offset:1024
	global_load_dwordx4 v[68:71], v[8:9], off offset:1024
	global_load_dwordx4 v[84:87], v[10:11], off offset:1024
	global_load_dwordx4 v[88:91], v[12:13], off offset:1024
	global_load_dwordx4 v[92:95], v[14:15], off offset:1024
	s_waitcnt lgkmcnt(0)
	v_mfma_f32_16x16x32_f16 v[48:51], v[64:67], v[72:75], v[48:51]
	s_barrier
	v_mfma_f32_16x16x32_f16 v[40:43], v[80:83], v[72:75], v[40:43]
	v_mfma_f32_16x16x32_f16 v[44:47], v[64:67], v[76:79], v[44:47]
	ds_read_b128 v[64:67], v34 offset:32768
	ds_read_b128 v[72:75], v34 offset:36864
	v_mfma_f32_16x16x32_f16 v[52:55], v[80:83], v[76:79], v[52:55]
	ds_read_b128 v[76:79], v21 offset:16384
	ds_read_b128 v[80:83], v21 offset:20480
	s_waitcnt lgkmcnt(1)
	v_mfma_f32_16x16x32_f16 v[48:51], v[64:67], v[76:79], v[48:51]
	v_mfma_f32_16x16x32_f16 v[40:43], v[72:75], v[76:79], v[40:43]
	s_waitcnt lgkmcnt(0)
	v_mfma_f32_16x16x32_f16 v[44:47], v[64:67], v[80:83], v[44:47]
	ds_read_b128 v[64:67], v36 offset:32768
	ds_read_b128 v[76:79], v36 offset:36864
	v_mfma_f32_16x16x32_f16 v[52:55], v[72:75], v[80:83], v[52:55]
	ds_read_b128 v[72:75], v23 offset:16384
	ds_read_b128 v[80:83], v23 offset:20480
	s_waitcnt lgkmcnt(1)
	v_mfma_f32_16x16x32_f16 v[48:51], v[64:67], v[72:75], v[48:51]
	v_mfma_f32_16x16x32_f16 v[40:43], v[76:79], v[72:75], v[40:43]
	s_waitcnt lgkmcnt(0)
	v_mfma_f32_16x16x32_f16 v[44:47], v[64:67], v[80:83], v[44:47]
	ds_read_b128 v[64:67], v37 offset:32768
	ds_read_b128 v[72:75], v37 offset:36864
	v_mfma_f32_16x16x32_f16 v[52:55], v[76:79], v[80:83], v[52:55]
	ds_read_b128 v[76:79], v24 offset:16384
	ds_read_b128 v[80:83], v24 offset:20480
	s_waitcnt lgkmcnt(1)
	v_mfma_f32_16x16x32_f16 v[48:51], v[64:67], v[76:79], v[48:51]
	v_mfma_f32_16x16x32_f16 v[40:43], v[72:75], v[76:79], v[40:43]
	s_waitcnt lgkmcnt(0)
	v_mfma_f32_16x16x32_f16 v[44:47], v[64:67], v[80:83], v[44:47]
	ds_read_b128 v[64:67], v38 offset:32768
	ds_read_b128 v[76:79], v22 offset:16384
	ds_read_b128 v[96:99], v38 offset:36864
	global_load_dwordx4 v[100:103], v[10:11], off offset:1280
	v_mfma_f32_16x16x32_f16 v[52:55], v[72:75], v[80:83], v[52:55]
	global_load_dwordx4 v[72:75], v[8:9], off offset:1280
	ds_read_b128 v[80:83], v22 offset:20480
	global_load_dwordx4 v[104:107], v[12:13], off offset:1280
	global_load_dwordx4 v[108:111], v[14:15], off offset:1280
	s_waitcnt lgkmcnt(2)
	v_mfma_f32_16x16x32_f16 v[48:51], v[64:67], v[76:79], v[48:51]
	s_waitcnt lgkmcnt(1)
	v_mfma_f32_16x16x32_f16 v[40:43], v[96:99], v[76:79], v[40:43]
	global_load_dwordx4 v[76:79], v[16:17], off offset:1280
	global_load_dwordx4 v[112:115], v[18:19], off offset:1280
	s_waitcnt vmcnt(11)
	ds_write_b128 v20, v[56:59]
	s_waitcnt vmcnt(10)
	ds_write_b128 v20, v[60:63] offset:8192
	s_waitcnt vmcnt(9)
	ds_write_b128 v20, v[68:71] offset:32768
	s_waitcnt vmcnt(8)
	ds_write_b128 v20, v[84:87] offset:40960
	s_waitcnt vmcnt(7)
	ds_write_b128 v20, v[88:91] offset:49152
	s_waitcnt vmcnt(6)
	ds_write_b128 v20, v[92:95] offset:57344
	s_waitcnt lgkmcnt(0)
	s_barrier
	ds_read_b128 v[56:59], v31 offset:32768
	v_mfma_f32_16x16x32_f16 v[44:47], v[64:67], v[80:83], v[44:47]
	ds_read_b128 v[60:63], v31 offset:36864
	ds_read_b128 v[64:67], v21
	ds_read_b128 v[68:71], v21 offset:4096
	v_mfma_f32_16x16x32_f16 v[52:55], v[96:99], v[80:83], v[52:55]
	s_waitcnt lgkmcnt(1)
	v_mfma_f32_16x16x32_f16 v[48:51], v[56:59], v[64:67], v[48:51]
	v_mfma_f32_16x16x32_f16 v[40:43], v[60:63], v[64:67], v[40:43]
	s_waitcnt lgkmcnt(0)
	v_mfma_f32_16x16x32_f16 v[44:47], v[56:59], v[68:71], v[44:47]
	ds_read_b128 v[56:59], v32 offset:32768
	ds_read_b128 v[64:67], v32 offset:36864
	v_mfma_f32_16x16x32_f16 v[52:55], v[60:63], v[68:71], v[52:55]
	ds_read_b128 v[60:63], v23
	ds_read_b128 v[68:71], v23 offset:4096
	s_waitcnt lgkmcnt(1)
	v_mfma_f32_16x16x32_f16 v[48:51], v[56:59], v[60:63], v[48:51]
	v_mfma_f32_16x16x32_f16 v[40:43], v[64:67], v[60:63], v[40:43]
	s_waitcnt lgkmcnt(0)
	v_mfma_f32_16x16x32_f16 v[44:47], v[56:59], v[68:71], v[44:47]
	ds_read_b128 v[56:59], v35 offset:32768
	ds_read_b128 v[60:63], v35 offset:36864
	v_mfma_f32_16x16x32_f16 v[52:55], v[64:67], v[68:71], v[52:55]
	ds_read_b128 v[64:67], v24
	ds_read_b128 v[68:71], v24 offset:4096
	s_waitcnt vmcnt(4)
	ds_write_b128 v116, v[72:75] offset:32768
	s_waitcnt lgkmcnt(2)
	v_mfma_f32_16x16x32_f16 v[48:51], v[56:59], v[64:67], v[48:51]
	v_mfma_f32_16x16x32_f16 v[40:43], v[60:63], v[64:67], v[40:43]
	ds_read_b128 v[64:67], v33 offset:32768
	s_waitcnt lgkmcnt(2)
	v_mfma_f32_16x16x32_f16 v[44:47], v[56:59], v[68:71], v[44:47]
	ds_read_b128 v[56:59], v22
	ds_read_b128 v[72:75], v33 offset:36864
	ds_write_b128 v116, v[100:103] offset:40960
	s_waitcnt vmcnt(3)
	ds_write_b128 v116, v[104:107] offset:49152
	v_mfma_f32_16x16x32_f16 v[52:55], v[60:63], v[68:71], v[52:55]
	ds_read_b128 v[60:63], v22 offset:4096
	s_waitcnt vmcnt(2)
	ds_write_b128 v116, v[108:111] offset:57344
	s_waitcnt vmcnt(1)
	ds_write_b128 v20, v[76:79] offset:16384
	s_waitcnt vmcnt(0)
	ds_write_b128 v20, v[112:115] offset:24576
	s_waitcnt lgkmcnt(7)
	v_mfma_f32_16x16x32_f16 v[48:51], v[64:67], v[56:59], v[48:51]
	s_waitcnt lgkmcnt(6)
	v_mfma_f32_16x16x32_f16 v[40:43], v[72:75], v[56:59], v[40:43]
	global_load_dwordx4 v[56:59], v[16:17], off offset:1536
	global_load_dwordx4 v[68:71], v[18:19], off offset:1536
	global_load_dwordx4 v[76:79], v[8:9], off offset:1536
	global_load_dwordx4 v[80:83], v[10:11], off offset:1536
	s_waitcnt lgkmcnt(3)
	v_mfma_f32_16x16x32_f16 v[44:47], v[64:67], v[60:63], v[44:47]
	global_load_dwordx4 v[64:67], v[12:13], off offset:1536
	global_load_dwordx4 v[84:87], v[14:15], off offset:1536
	s_waitcnt lgkmcnt(0)
	s_barrier
	ds_read_b128 v[88:91], v34 offset:32768
	v_mfma_f32_16x16x32_f16 v[52:55], v[72:75], v[60:63], v[52:55]
	ds_read_b128 v[60:63], v34 offset:36864
	ds_read_b128 v[72:75], v21 offset:16384
	ds_read_b128 v[92:95], v21 offset:20480
	s_waitcnt lgkmcnt(1)
	v_mfma_f32_16x16x32_f16 v[48:51], v[88:91], v[72:75], v[48:51]
	v_mfma_f32_16x16x32_f16 v[40:43], v[60:63], v[72:75], v[40:43]
	ds_read_b128 v[72:75], v36 offset:32768
	s_waitcnt lgkmcnt(1)
	v_mfma_f32_16x16x32_f16 v[44:47], v[88:91], v[92:95], v[44:47]
	v_mfma_f32_16x16x32_f16 v[52:55], v[60:63], v[92:95], v[52:55]
	ds_read_b128 v[60:63], v36 offset:36864
	ds_read_b128 v[88:91], v23 offset:16384
	ds_read_b128 v[92:95], v23 offset:20480
	s_waitcnt lgkmcnt(1)
	v_mfma_f32_16x16x32_f16 v[48:51], v[72:75], v[88:91], v[48:51]
	v_mfma_f32_16x16x32_f16 v[40:43], v[60:63], v[88:91], v[40:43]
	s_waitcnt lgkmcnt(0)
	v_mfma_f32_16x16x32_f16 v[44:47], v[72:75], v[92:95], v[44:47]
	ds_read_b128 v[72:75], v37 offset:32768
	ds_read_b128 v[88:91], v37 offset:36864
	v_mfma_f32_16x16x32_f16 v[52:55], v[60:63], v[92:95], v[52:55]
	ds_read_b128 v[60:63], v24 offset:16384
	ds_read_b128 v[92:95], v24 offset:20480
	s_waitcnt lgkmcnt(1)
	v_mfma_f32_16x16x32_f16 v[48:51], v[72:75], v[60:63], v[48:51]
	v_mfma_f32_16x16x32_f16 v[40:43], v[88:91], v[60:63], v[40:43]
	s_waitcnt lgkmcnt(0)
	v_mfma_f32_16x16x32_f16 v[44:47], v[72:75], v[92:95], v[44:47]
	ds_read_b128 v[60:63], v38 offset:32768
	ds_read_b128 v[72:75], v38 offset:36864
	v_mfma_f32_16x16x32_f16 v[52:55], v[88:91], v[92:95], v[52:55]
	ds_read_b128 v[88:91], v22 offset:16384
	ds_read_b128 v[92:95], v22 offset:20480
	global_load_dwordx4 v[96:99], v[16:17], off offset:1792
	global_load_dwordx4 v[100:103], v[18:19], off offset:1792
	s_waitcnt lgkmcnt(1)
	v_mfma_f32_16x16x32_f16 v[48:51], v[60:63], v[88:91], v[48:51]
	v_mfma_f32_16x16x32_f16 v[16:19], v[72:75], v[88:91], v[40:43]
	s_nop 2
	global_load_dwordx4 v[40:43], v[8:9], off offset:1792
	global_load_dwordx4 v[88:91], v[10:11], off offset:1792
	global_load_dwordx4 v[104:107], v[12:13], off offset:1792
	global_load_dwordx4 v[108:111], v[14:15], off offset:1792
	s_waitcnt vmcnt(11)
	ds_write_b128 v20, v[56:59]
	s_waitcnt vmcnt(10)
	ds_write_b128 v20, v[68:71] offset:8192
	s_waitcnt vmcnt(9)
	ds_write_b128 v20, v[76:79] offset:32768
	s_waitcnt vmcnt(8)
	ds_write_b128 v20, v[80:83] offset:40960
	s_waitcnt vmcnt(7)
	ds_write_b128 v20, v[64:67] offset:49152
	s_waitcnt vmcnt(6)
	ds_write_b128 v20, v[84:87] offset:57344
	s_waitcnt lgkmcnt(0)
	s_barrier
	ds_read_b128 v[12:15], v31 offset:32768
	v_mfma_f32_16x16x32_f16 v[8:11], v[60:63], v[92:95], v[44:47]
	v_mfma_f32_16x16x32_f16 v[44:47], v[72:75], v[92:95], v[52:55]
	s_nop 2
	ds_read_b128 v[52:55], v31 offset:36864
	ds_read_b128 v[56:59], v21
	ds_read_b128 v[60:63], v21 offset:4096
	s_waitcnt lgkmcnt(1)
	v_mfma_f32_16x16x32_f16 v[48:51], v[12:15], v[56:59], v[48:51]
	v_mfma_f32_16x16x32_f16 v[16:19], v[52:55], v[56:59], v[16:19]
	s_waitcnt lgkmcnt(0)
	v_mfma_f32_16x16x32_f16 v[8:11], v[12:15], v[60:63], v[8:11]
	ds_read_b128 v[12:15], v32 offset:32768
	ds_read_b128 v[56:59], v32 offset:36864
	v_mfma_f32_16x16x32_f16 v[44:47], v[52:55], v[60:63], v[44:47]
	ds_read_b128 v[52:55], v23
	ds_read_b128 v[60:63], v23 offset:4096
	s_waitcnt lgkmcnt(1)
	v_mfma_f32_16x16x32_f16 v[48:51], v[12:15], v[52:55], v[48:51]
	v_mfma_f32_16x16x32_f16 v[16:19], v[56:59], v[52:55], v[16:19]
	s_waitcnt lgkmcnt(0)
	v_mfma_f32_16x16x32_f16 v[8:11], v[12:15], v[60:63], v[8:11]
	ds_read_b128 v[12:15], v35 offset:32768
	ds_read_b128 v[52:55], v35 offset:36864
	v_mfma_f32_16x16x32_f16 v[44:47], v[56:59], v[60:63], v[44:47]
	ds_read_b128 v[56:59], v24
	ds_read_b128 v[60:63], v24 offset:4096
	s_waitcnt lgkmcnt(1)
	v_mfma_f32_16x16x32_f16 v[48:51], v[12:15], v[56:59], v[48:51]
	s_waitcnt lgkmcnt(0)
	v_mfma_f32_16x16x32_f16 v[8:11], v[12:15], v[60:63], v[8:11]
	ds_read_b128 v[12:15], v33 offset:32768
	v_mfma_f32_16x16x32_f16 v[16:19], v[52:55], v[56:59], v[16:19]
	v_mfma_f32_16x16x32_f16 v[44:47], v[52:55], v[60:63], v[44:47]
	ds_read_b128 v[52:55], v33 offset:36864
	ds_read_b128 v[56:59], v22
	ds_read_b128 v[60:63], v22 offset:4096
	s_waitcnt vmcnt(5)
	ds_write_b128 v20, v[96:99] offset:16384
	s_waitcnt vmcnt(4)
	ds_write_b128 v20, v[100:103] offset:24576
	s_waitcnt lgkmcnt(3)
	v_mfma_f32_16x16x32_f16 v[48:51], v[12:15], v[56:59], v[48:51]
	s_waitcnt lgkmcnt(2)
	v_mfma_f32_16x16x32_f16 v[8:11], v[12:15], v[60:63], v[8:11]
	v_add_u32_e32 v12, 0x10000, v20
	s_waitcnt vmcnt(3)
	ds_write_b128 v12, v[40:43]
	s_waitcnt vmcnt(2)
	ds_write_b128 v12, v[88:91] offset:8192
	s_waitcnt vmcnt(1)
	ds_write_b128 v12, v[104:107] offset:16384
	s_waitcnt vmcnt(0)
	ds_write_b128 v12, v[108:111] offset:24576
	s_waitcnt lgkmcnt(0)
	s_barrier
	ds_read_b128 v[12:15], v34 offset:32768
	v_mfma_f32_16x16x32_f16 v[16:19], v[52:55], v[56:59], v[16:19]
	v_mfma_f32_16x16x32_f16 v[40:43], v[52:55], v[60:63], v[44:47]
	ds_read_b128 v[32:35], v34 offset:36864
	s_nop 1
	ds_read_b128 v[44:47], v21 offset:16384
	ds_read_b128 v[52:55], v21 offset:20480
	s_waitcnt lgkmcnt(1)
	v_mfma_f32_16x16x32_f16 v[48:51], v[12:15], v[44:47], v[48:51]
	s_waitcnt lgkmcnt(0)
	v_mfma_f32_16x16x32_f16 v[8:11], v[12:15], v[52:55], v[8:11]
	ds_read_b128 v[12:15], v36 offset:32768
	v_mfma_f32_16x16x32_f16 v[16:19], v[32:35], v[44:47], v[16:19]
	v_mfma_f32_16x16x32_f16 v[32:35], v[32:35], v[52:55], v[40:43]
	s_nop 2
	ds_read_b128 v[40:43], v36 offset:36864
	ds_read_b128 v[44:47], v23 offset:16384
	ds_read_b128 v[52:55], v23 offset:20480
	s_waitcnt lgkmcnt(1)
	v_mfma_f32_16x16x32_f16 v[48:51], v[12:15], v[44:47], v[48:51]
	s_waitcnt lgkmcnt(0)
	v_mfma_f32_16x16x32_f16 v[8:11], v[12:15], v[52:55], v[8:11]
	ds_read_b128 v[12:15], v37 offset:32768
	v_mfma_f32_16x16x32_f16 v[16:19], v[40:43], v[44:47], v[16:19]
	v_mfma_f32_16x16x32_f16 v[32:35], v[40:43], v[52:55], v[32:35]
	ds_read_b128 v[40:43], v37 offset:36864
	ds_read_b128 v[44:47], v24 offset:16384
	ds_read_b128 v[52:55], v24 offset:20480
	v_lshlrev_b32_e32 v24, 6, v30
	s_waitcnt lgkmcnt(1)
	v_mfma_f32_16x16x32_f16 v[48:51], v[12:15], v[44:47], v[48:51]
	s_waitcnt lgkmcnt(0)
	v_mfma_f32_16x16x32_f16 v[8:11], v[12:15], v[52:55], v[8:11]
	ds_read_b128 v[12:15], v38 offset:32768
	v_mfma_f32_16x16x32_f16 v[16:19], v[40:43], v[44:47], v[16:19]
	v_mfma_f32_16x16x32_f16 v[32:35], v[40:43], v[52:55], v[32:35]
	ds_read_b128 v[36:39], v38 offset:36864
	ds_read_b128 v[40:43], v22 offset:16384
	ds_read_b128 v[44:47], v22 offset:20480
	s_waitcnt lgkmcnt(1)
	v_mfma_f32_16x16x32_f16 v[20:23], v[12:15], v[40:43], v[48:51]
	s_waitcnt lgkmcnt(0)
	v_mfma_f32_16x16x32_f16 v[12:15], v[12:15], v[44:47], v[8:11]
	s_nop 2
	v_lshl_add_u64 v[8:9], s[0:1], 0, v[24:25]
	v_lshlrev_b32_e32 v24, 3, v29
	v_mfma_f32_16x16x32_f16 v[16:19], v[36:39], v[40:43], v[16:19]
	v_lshl_add_u64 v[30:31], v[8:9], 0, v[24:25]
	v_mfma_f32_16x16x32_f16 v[8:11], v[36:39], v[44:47], v[32:35]
	v_mbcnt_lo_u32_b32 v196, -1, 0
	v_mbcnt_hi_u32_b32 v196, -1, v196
	v_and_b32_e32 v197, 15, v196
	v_lshrrev_b32_e32 v198, 4, v196
	v_lshrrev_b32_e32 v222, 10, v116
	s_nop 0
	v_readfirstlane_b32 s36, v222
	s_nop 3
	s_and_b32 s36, s36, 7
	s_mulk_i32 s36, 0x500
	s_add_u32 s36, s36, 0x8000
	v_mul_u32_u24_e32 v199, 0x50, v197
	v_lshl_add_u32 v199, v198, 3, v199
	v_add_u32_e32 v199, s36, v199
	v_lshrrev_b32_e32 v200, 2, v196
	v_and_b32_e32 v201, 3, v196
	v_mul_u32_u24_e32 v202, 0x50, v200
	v_lshl_add_u32 v202, v201, 4, v202
	v_add_u32_e32 v202, s36, v202
	v_lshlrev_b32_e32 v203, 2, v200
	v_add_u32_e32 v204, 32, v203
	v_lshlrev_b32_e32 v220, 4, v201
	v_mov_b32_e32 v221, 0
	v_sub_u32_e32 v205, v27, v197
	v_add_u32_e32 v205, v205, v200
	s_mov_b64 s[0:1], exec
	s_cbranch_execz .LBB7_9
	v_mov_b32_e32 v29, v25
	v_lshl_add_u64 v[24:25], s[2:3], 0, v[28:29]
	global_load_dword v24, v[24:25], off
	s_nop 0
	v_add_f32_e32 v16, v0, v16
	v_add_f32_e32 v17, v1, v17
	v_add_f32_e32 v18, v2, v18
	v_add_f32_e32 v19, v3, v19
	v_add_f32_e32 v20, v4, v20
	v_add_f32_e32 v21, v5, v21
	v_max_f32_e32 v25, 0, v16
	v_max_f32_e32 v28, 0, v17
	v_max_f32_e32 v18, 0, v18
	v_max_f32_e32 v19, 0, v19
	v_add_f32_e32 v22, v6, v22
	v_add_f32_e32 v23, v7, v23
	v_max_f32_e32 v20, 0, v20
	v_max_f32_e32 v21, 0, v21
	v_cvt_pk_f16_f32 v19, v18, v19
	v_cvt_pk_f16_f32 v18, v25, v28
	v_max_f32_e32 v22, 0, v22
	v_max_f32_e32 v23, 0, v23
	v_cvt_pk_f16_f32 v16, v20, v21
	v_cvt_pk_f16_f32 v17, v22, v23
	s_waitcnt vmcnt(0)
	v_ashrrev_i32_e32 v25, 31, v24
	v_lshlrev_b64 v[20:21], 11, v[24:25]
	v_lshl_add_u64 v[20:21], v[30:31], 0, v[20:21]
	ds_write_b64 v199, v[16:17]
	ds_write_b64 v199, v[18:19] offset:32
	s_waitcnt lgkmcnt(0)
	ds_read_b128 v[208:211], v202
	ds_bpermute_b32 v216, v203, v20
	ds_bpermute_b32 v217, v203, v21
	v_add_u32_e32 v222, 0, v205
	v_cmp_gt_u32_e64 s[38:39], s4, v222
	s_waitcnt lgkmcnt(0)
	v_lshl_add_u64 v[216:217], v[216:217], 0, v[220:221]
	s_mov_b64 s[42:43], exec
	s_and_b64 exec, s[42:43], s[38:39]
	global_store_dwordx4 v[216:217], v[208:211], off
	s_mov_b64 exec, s[42:43]
.LBB7_9:
	s_or_b64 exec, exec, s[0:1]
	s_nop 2
	v_or_b32_e32 v16, 16, v27
	v_cmp_gt_u32_e32 vcc, s4, v16
	s_mov_b64 s[0:1], exec
	s_cbranch_execz .LBB7_11
	v_add_f32_e32 v5, v5, v13
	v_ashrrev_i32_e32 v27, 31, v26
	v_add_f32_e32 v4, v4, v12
	v_max_f32_e32 v12, 0, v5
	v_add_f32_e32 v5, v6, v14
	v_add_f32_e32 v6, v7, v15
	v_lshlrev_b64 v[16:17], 11, v[26:27]
	v_max_f32_e32 v4, 0, v4
	v_max_f32_e32 v5, 0, v5
	v_max_f32_e32 v6, 0, v6
	v_lshl_add_u64 v[16:17], v[30:31], 0, v[16:17]
	v_cvt_pk_f16_f32 v5, v5, v6
	v_cvt_pk_f16_f32 v4, v4, v12
	v_add_f32_e32 v1, v1, v9
	ds_write_b64 v199, v[4:5]
	v_add_f32_e32 v0, v0, v8
	v_max_f32_e32 v4, 0, v1
	v_add_f32_e32 v1, v2, v10
	v_add_f32_e32 v2, v3, v11
	v_max_f32_e32 v0, 0, v0
	v_max_f32_e32 v1, 0, v1
	v_max_f32_e32 v2, 0, v2
	v_cvt_pk_f16_f32 v1, v1, v2
	v_cvt_pk_f16_f32 v0, v0, v4
	ds_write_b64 v199, v[0:1] offset:32
	s_waitcnt lgkmcnt(0)
	ds_read_b128 v[208:211], v202
	ds_bpermute_b32 v216, v203, v16
	ds_bpermute_b32 v217, v203, v17
	v_add_u32_e32 v222, 16, v205
	v_cmp_gt_u32_e64 s[38:39], s4, v222
	s_waitcnt lgkmcnt(0)
	v_lshl_add_u64 v[216:217], v[216:217], 0, v[220:221]
	s_mov_b64 s[42:43], exec
	s_and_b64 exec, s[42:43], s[38:39]
	global_store_dwordx4 v[216:217], v[208:211], off
	s_mov_b64 exec, s[42:43]

	.amdhsa_kernel _Z11gemm_kernelILi1ELi64ELi128ELi128ELi2ELi4ELi2ELi2ELi128EEvPKDF16_PDF16_PKiS4_S1_S1_PKf
		.amdhsa_group_segment_fixed_size 0
		.amdhsa_private_segment_fixed_size 0
		.amdhsa_kernarg_size 56
		.amdhsa_user_sgpr_count 2
		.amdhsa_user_sgpr_dispatch_ptr 0
		.amdhsa_user_sgpr_queue_ptr 0
		.amdhsa_user_sgpr_kernarg_segment_ptr 1
		.amdhsa_user_sgpr_dispatch_id 0
		.amdhsa_user_sgpr_kernarg_preload_length 0
		.amdhsa_user_sgpr_kernarg_preload_offset 0
		.amdhsa_user_sgpr_private_segment_size 0
		.amdhsa_uses_dynamic_stack 0
		.amdhsa_enable_private_segment 0
		.amdhsa_system_sgpr_workgroup_id_x 1
		.amdhsa_system_sgpr_workgroup_id_y 0
		.amdhsa_system_sgpr_workgroup_id_z 0
		.amdhsa_system_sgpr_workgroup_info 0
		.amdhsa_system_vgpr_workitem_id 0
		.amdhsa_next_free_vgpr 224
		.amdhsa_next_free_sgpr 44
		.amdhsa_accum_offset 224
		.amdhsa_reserve_vcc 1
		.amdhsa_float_round_mode_32 0
		.amdhsa_float_round_mode_16_64 0
		.amdhsa_float_denorm_mode_32 3
		.amdhsa_float_denorm_mode_16_64 3
		.amdhsa_dx10_clamp 1
		.amdhsa_ieee_mode 1
		.amdhsa_fp16_overflow 0
		.amdhsa_tg_split 0
		.amdhsa_exception_fp_ieee_invalid_op 0
		.amdhsa_exception_fp_denorm_src 0
		.amdhsa_exception_fp_ieee_div_zero 0
		.amdhsa_exception_fp_ieee_overflow 0
		.amdhsa_exception_fp_ieee_underflow 0
		.amdhsa_exception_fp_ieee_inexact 0
		.amdhsa_exception_int_div_zero 0
	.end_amdhsa_kernel

amdhsa.kernels:
  - .agpr_count:     0
    .args:
      - .actual_access:  read_only
        .address_space:  global
        .offset:         0
        .size:           8
        .value_kind:     global_buffer
      - .actual_access:  read_only
        .address_space:  global
        .offset:         8
        .size:           8
        .value_kind:     global_buffer
      - .actual_access:  read_only
        .address_space:  global
        .offset:         16
        .size:           8
        .value_kind:     global_buffer
      - .actual_access:  read_only
        .address_space:  global
        .offset:         24
        .size:           8
        .value_kind:     global_buffer
      - .actual_access:  read_only
        .address_space:  global
        .offset:         32
        .size:           8
        .value_kind:     global_buffer
      - .actual_access:  read_only
        .address_space:  global
        .offset:         40
        .size:           8
        .value_kind:     global_buffer
      - .actual_access:  read_only
        .address_space:  global
        .offset:         48
        .size:           8
        .value_kind:     global_buffer
      - .actual_access:  read_only
        .address_space:  global
        .offset:         56
        .size:           8
        .value_kind:     global_buffer
      - .actual_access:  write_only
        .address_space:  global
        .offset:         64
        .size:           8
        .value_kind:     global_buffer
    .group_segment_fixed_size: 16832
    .kernarg_segment_align: 8
    .kernarg_segment_size: 72
    .language:       OpenCL C
    .language_version:
      - 2
      - 0
    .max_flat_workgroup_size: 256
    .name:           _Z12front_kernelPKiS0_S0_PKfS2_S2_S2_S2_Pc
    .private_segment_fixed_size: 0
    .sgpr_count:     106
    .sgpr_spill_count: 398
    .symbol:         _Z12front_kernelPKiS0_S0_PKfS2_S2_S2_S2_Pc.kd
    .uniform_work_group_size: 1
    .uses_dynamic_stack: false
    .vgpr_count:     78
    .vgpr_spill_count: 0
    .wavefront_size: 64
  - .agpr_count:     0
    .args:
      - .actual_access:  read_only
        .address_space:  global
        .offset:         0
        .size:           8
        .value_kind:     global_buffer
      - .actual_access:  read_only
        .address_space:  global
        .offset:         8
        .size:           8
        .value_kind:     global_buffer
      - .actual_access:  read_only
        .address_space:  global
        .offset:         16
        .size:           8
        .value_kind:     global_buffer
      - .actual_access:  write_only
        .address_space:  global
        .offset:         24
        .size:           8
        .value_kind:     global_buffer
    .group_segment_fixed_size: 0
    .kernarg_segment_align: 8
    .kernarg_segment_size: 32
    .language:       OpenCL C
    .language_version:
      - 2
      - 0
    .max_flat_workgroup_size: 256
    .name:           _Z12final_kernelPKDF16_PKfS2_Pf
    .private_segment_fixed_size: 0
    .sgpr_count:     14
    .sgpr_spill_count: 0
    .symbol:         _Z12final_kernelPKDF16_PKfS2_Pf.kd
    .uniform_work_group_size: 1
    .uses_dynamic_stack: false
    .vgpr_count:     40
    .vgpr_spill_count: 0
    .wavefront_size: 64
  - .agpr_count:     0
    .args:
      - .address_space:  global
        .offset:         0
        .size:           8
        .value_kind:     global_buffer
      - .actual_access:  write_only
        .address_space:  global
        .offset:         8
        .size:           8
        .value_kind:     global_buffer
      - .actual_access:  read_only
        .address_space:  global
        .offset:         16
        .size:           8
        .value_kind:     global_buffer
      - .actual_access:  read_only
        .address_space:  global
        .offset:         24
        .size:           8
        .value_kind:     global_buffer
      - .address_space:  global
        .offset:         32
        .size:           8
        .value_kind:     global_buffer
      - .address_space:  global
        .offset:         40
        .size:           8
        .value_kind:     global_buffer
      - .actual_access:  read_only
        .address_space:  global
        .offset:         48
        .size:           8
        .value_kind:     global_buffer
      - .offset:         56
        .size:           4
        .value_kind:     by_value
      - .actual_access:  read_only
        .address_space:  global
        .offset:         64
        .size:           8
        .value_kind:     global_buffer
      - .actual_access:  write_only
        .address_space:  global
        .offset:         72
        .size:           8
        .value_kind:     global_buffer
    .group_segment_fixed_size: 0
    .kernarg_segment_align: 8
    .kernarg_segment_size: 80
    .language:       OpenCL C
    .language_version:
      - 2
      - 0
    .max_flat_workgroup_size: 512
    .name:           _Z16gemm_glds_kernelILi2EEvPKDF16_PDF16_PKiS4_S1_S1_PKfiS6_Pc
    .private_segment_fixed_size: 0
    .sgpr_count:     50
    .sgpr_spill_count: 0
    .symbol:         _Z16gemm_glds_kernelILi2EEvPKDF16_PDF16_PKiS4_S1_S1_PKfiS6_Pc.kd
    .uniform_work_group_size: 1
    .uses_dynamic_stack: false
    .vgpr_count:     186
    .vgpr_spill_count: 0
    .wavefront_size: 64
  - .agpr_count:     0
    .args:
      - .actual_access:  read_only
        .address_space:  global
        .offset:         0
        .size:           8
        .value_kind:     global_buffer
      - .actual_access:  write_only
        .address_space:  global
        .offset:         8
        .size:           8
        .value_kind:     global_buffer
      - .actual_access:  read_only
        .address_space:  global
        .offset:         16
        .size:           8
        .value_kind:     global_buffer
      - .actual_access:  read_only
        .address_space:  global
        .offset:         24
        .size:           8
        .value_kind:     global_buffer
      - .actual_access:  read_only
        .address_space:  global
        .offset:         32
        .size:           8
        .value_kind:     global_buffer
      - .actual_access:  read_only
        .address_space:  global
        .offset:         40
        .size:           8
        .value_kind:     global_buffer
      - .actual_access:  read_only
        .address_space:  global
        .offset:         48
        .size:           8
        .value_kind:     global_buffer
    .group_segment_fixed_size: 0
    .kernarg_segment_align: 8
    .kernarg_segment_size: 56
    .language:       OpenCL C
    .language_version:
      - 2
      - 0
    .max_flat_workgroup_size: 512
    .name:           _Z11gemm_kernelILi0ELi192ELi256ELi128ELi2ELi4ELi2ELi2ELi64EEvPKDF16_PDF16_PKiS4_S1_S1_PKf
    .private_segment_fixed_size: 0
    .sgpr_count:     30
    .sgpr_spill_count: 0
    .symbol:         _Z11gemm_kernelILi0ELi192ELi256ELi128ELi2ELi4ELi2ELi2ELi64EEvPKDF16_PDF16_PKiS4_S1_S1_PKf.kd
    .uniform_work_group_size: 1
    .uses_dynamic_stack: false
    .vgpr_count:     254
    .vgpr_spill_count: 0
    .wavefront_size: 64
  - .agpr_count:     0
    .args:
      - .actual_access:  read_only
        .address_space:  global
        .offset:         0
        .size:           8
        .value_kind:     global_buffer
      - .actual_access:  write_only
        .address_space:  global
        .offset:         8
        .size:           8
        .value_kind:     global_buffer
      - .actual_access:  read_only
        .address_space:  global
        .offset:         16
        .size:           8
        .value_kind:     global_buffer
      - .actual_access:  read_only
        .address_space:  global
        .offset:         24
        .size:           8
        .value_kind:     global_buffer
      - .actual_access:  read_only
        .address_space:  global
        .offset:         32
        .size:           8
        .value_kind:     global_buffer
      - .actual_access:  read_only
        .address_space:  global
        .offset:         40
        .size:           8
        .value_kind:     global_buffer
      - .actual_access:  read_only
        .address_space:  global
        .offset:         48
        .size:           8
        .value_kind:     global_buffer
    .group_segment_fixed_size: 0
    .kernarg_segment_align: 8
    .kernarg_segment_size: 56
    .language:       OpenCL C
    .language_version:
      - 2
      - 0
    .max_flat_workgroup_size: 512
    .name:           _Z11gemm_kernelILi0ELi96ELi256ELi128ELi2ELi4ELi2ELi2ELi64EEvPKDF16_PDF16_PKiS4_S1_S1_PKf
    .private_segment_fixed_size: 0
    .sgpr_count:     32
    .sgpr_spill_count: 0
    .symbol:         _Z11gemm_kernelILi0ELi96ELi256ELi128ELi2ELi4ELi2ELi2ELi64EEvPKDF16_PDF16_PKiS4_S1_S1_PKf.kd
    .uniform_work_group_size: 1
    .uses_dynamic_stack: false
    .vgpr_count:     224
    .vgpr_spill_count: 0
    .wavefront_size: 64
  - .agpr_count:     0
    .args:
      - .address_space:  global
        .offset:         0
        .size:           8
        .value_kind:     global_buffer
      - .actual_access:  write_only
        .address_space:  global
        .offset:         8
        .size:           8
        .value_kind:     global_buffer
      - .actual_access:  read_only
        .address_space:  global
        .offset:         16
        .size:           8
        .value_kind:     global_buffer
      - .actual_access:  read_only
        .address_space:  global
        .offset:         24
        .size:           8
        .value_kind:     global_buffer
      - .address_space:  global
        .offset:         32
        .size:           8
        .value_kind:     global_buffer
      - .address_space:  global
        .offset:         40
        .size:           8
        .value_kind:     global_buffer
      - .actual_access:  read_only
        .address_space:  global
        .offset:         48
        .size:           8
        .value_kind:     global_buffer
    .group_segment_fixed_size: 0
    .kernarg_segment_align: 8
    .kernarg_segment_size: 56
    .language:       OpenCL C
    .language_version:
      - 2
      - 0
    .max_flat_workgroup_size: 256
    .name:           _Z15gemm_dma_kernelILi0ELi96ELi128ELi64ELi2ELi2ELi3EEvPKDF16_PDF16_PKiS4_S1_S1_PKf
    .private_segment_fixed_size: 0
    .sgpr_count:     33
    .sgpr_spill_count: 0
    .symbol:         _Z15gemm_dma_kernelILi0ELi96ELi128ELi64ELi2ELi2ELi3EEvPKDF16_PDF16_PKiS4_S1_S1_PKf.kd
    .uniform_work_group_size: 1
    .uses_dynamic_stack: false
    .vgpr_count:     224
    .vgpr_spill_count: 0
    .wavefront_size: 64
  - .agpr_count:     0
    .args:
      - .actual_access:  read_only
        .address_space:  global
        .offset:         0
        .size:           8
        .value_kind:     global_buffer
      - .actual_access:  write_only
        .address_space:  global
        .offset:         8
        .size:           8
        .value_kind:     global_buffer
      - .actual_access:  read_only
        .address_space:  global
        .offset:         16
        .size:           8
        .value_kind:     global_buffer
      - .actual_access:  read_only
        .address_space:  global
        .offset:         24
        .size:           8
        .value_kind:     global_buffer
      - .actual_access:  read_only
        .address_space:  global
        .offset:         32
        .size:           8
        .value_kind:     global_buffer
      - .actual_access:  read_only
        .address_space:  global
        .offset:         40
        .size:           8
        .value_kind:     global_buffer
      - .actual_access:  read_only
        .address_space:  global
        .offset:         48
        .size:           8
        .value_kind:     global_buffer
    .group_segment_fixed_size: 0
    .kernarg_segment_align: 8
    .kernarg_segment_size: 56
    .language:       OpenCL C
    .language_version:
      - 2
      - 0
    .max_flat_workgroup_size: 256
    .name:           _Z11gemm_kernelILi0ELi48ELi128ELi64ELi1ELi4ELi2ELi2ELi128EEvPKDF16_PDF16_PKiS4_S1_S1_PKf
    .private_segment_fixed_size: 0
    .sgpr_count:     30
    .sgpr_spill_count: 0
    .symbol:         _Z11gemm_kernelILi0ELi48ELi128ELi64ELi1ELi4ELi2ELi2ELi128EEvPKDF16_PDF16_PKiS4_S1_S1_PKf.kd
    .uniform_work_group_size: 1
    .uses_dynamic_stack: false
    .vgpr_count:     224
    .vgpr_spill_count: 0
    .wavefront_size: 64
  - .agpr_count:     0
    .args:
      - .actual_access:  read_only
        .address_space:  global
        .offset:         0
        .size:           8
        .value_kind:     global_buffer
      - .actual_access:  write_only
        .address_space:  global
        .offset:         8
        .size:           8
        .value_kind:     global_buffer
      - .actual_access:  read_only
        .address_space:  global
        .offset:         16
        .size:           8
        .value_kind:     global_buffer
      - .actual_access:  read_only
        .address_space:  global
        .offset:         24
        .size:           8
        .value_kind:     global_buffer
      - .actual_access:  read_only
        .address_space:  global
        .offset:         32
        .size:           8
        .value_kind:     global_buffer
      - .actual_access:  read_only
        .address_space:  global
        .offset:         40
        .size:           8
        .value_kind:     global_buffer
      - .actual_access:  read_only
        .address_space:  global
        .offset:         48
        .size:           8
        .value_kind:     global_buffer
    .group_segment_fixed_size: 0
    .kernarg_segment_align: 8
    .kernarg_segment_size: 56
    .language:       OpenCL C
    .language_version:
      - 2
      - 0
    .max_flat_workgroup_size: 512
    .name:           _Z11gemm_kernelILi1ELi64ELi128ELi128ELi2ELi4ELi2ELi2ELi128EEvPKDF16_PDF16_PKiS4_S1_S1_PKf
    .private_segment_fixed_size: 0
    .sgpr_count:     23
    .sgpr_spill_count: 0
    .symbol:         _Z11gemm_kernelILi1ELi64ELi128ELi128ELi2ELi4ELi2ELi2ELi128EEvPKDF16_PDF16_PKiS4_S1_S1_PKf.kd
    .uniform_work_group_size: 1
    .uses_dynamic_stack: false
    .vgpr_count:     224
    .vgpr_spill_count: 0
    .wavefront_size: 64
